# P11 gate loads (PROJ gate columns, read once) marked non-temporal
# baseline (speedup 1.0000x reference)
; __device__ __forceinline__ float sigmoidf_(float x) { return 1.0f / (1.0f + __expf(-x)); }
; __device__ __forceinline__ int fresh_lane() { int l; asm volatile("v_mbcnt_lo_u32_b32 %0, -1, 0\n\tv_mbcnt_hi_u32_b32 %0, -1, %0" : "=v"(l)); return l; }
;     __device__ __forceinline__ void operator()(AccMut acc, const Unit& u, int wr, int wc, int, int) const {
;         const int ln_ = fresh_lane(), fr = ln_ & 15, fq = ln_ >> 4;
;         const int row0 = u.pm * 256 + wr * 64 + fr, col0 = u.pn * 256 + wc * 32 + 8 * fq;
; #pragma unroll
;         for (int ai = 0; ai < 2; ++ai)
; #pragma unroll
;             for (int m = 0; m < 4; ++m) {
; #pragma unroll
;                 for (int bj = 0; bj < 2; ++bj) {
;                     const int row = row0 + ai * 128 + m * 16, col = col0 + bj * 128;
;                     const bf16* gp = PROJ + (size_t)row * DINP + GATE_OFF + col;
;                     float sc[8];
;                     if (u.seg < 2) {
;                         const v4u ga = *(const v4u*)(gp + u.seg * D), gb = *(const v4u*)(gp + (u.seg + 1) * D);
;                         const float la[8] = {bflo(ga.x), bfhi(ga.x), bflo(ga.y), bfhi(ga.y), bflo(ga.z), bfhi(ga.z), bflo(ga.w), bfhi(ga.w)};
;                         const float lb[8] = {bflo(gb.x), bfhi(gb.x), bflo(gb.y), bfhi(gb.y), bflo(gb.z), bfhi(gb.z), bflo(gb.w), bfhi(gb.w)};
; #pragma unroll
;                         for (int j = 0; j < 8; ++j) { const float ea = __expf(-fminf(fmaxf(la[j], -30.f), 30.f)), eb = __expf(-fminf(fmaxf(lb[j], -30.f), 30.f)); sc[j] = (1.0f + eb) * __builtin_amdgcn_rcpf(1.0f + ea); }
;                     } else {
;                         const v4u ga = *(const v4u*)(gp + 2 * D);
;                         const float la[8] = {bflo(ga.x), bfhi(ga.x), bflo(ga.y), bfhi(ga.y), bflo(ga.z), bfhi(ga.z), bflo(ga.w), bfhi(ga.w)};
; #pragma unroll
;                         for (int j = 0; j < 8; ++j) sc[j] = sigmoidf_(la[j]);
.LBB0_914:
	v_mbcnt_lo_u32_b32 v0, -1, 0
	v_mbcnt_hi_u32_b32 v0, -1, v0
	s_lshl_b32 s2, s24, 8
	v_ashrrev_i32_e32 v1, 1, v0
	v_and_b32_e32 v1, -8, v1
	v_and_or_b32 v0, v0, 15, s43
	s_or_b32 s2, s2, s44
	v_lshl_add_u32 v154, s22, 8, v0
	v_add_u32_e32 v150, s2, v1
	v_mov_b64_e32 v[0:1], s[8:9]
	v_mad_i64_i32 v[0:1], s[2:3], v154, s91, v[0:1]
	s_cmp_gt_u32 s50, 1
	v_lshl_add_u64 v[156:157], v[0:1], 0, s[56:57]
	v_ashrrev_i32_e32 v151, 31, v150
	s_cselect_b64 s[22:23], -1, 0
	v_lshl_add_u64 v[152:153], v[150:151], 1, v[156:157]
	s_mov_b64 s[6:7], -1
	s_and_b64 vcc, exec, s[22:23]
	s_cbranch_vccz .LBB0_916
	v_add_co_u32_e32 v0, vcc, 0x2000, v152
	s_mov_b64 s[6:7], 0
	s_nop 0
	v_addc_co_u32_e32 v1, vcc, 0, v153, vcc
	global_load_dwordx4 v[0:3], v[0:1], off nt
	s_waitcnt vmcnt(0)
	v_lshlrev_b32_e32 v6, 16, v1
	v_and_b32_e32 v7, 0xffff0000, v1
	v_lshlrev_b32_e32 v158, 16, v3
	v_and_b32_e32 v159, 0xffff0000, v3
	v_lshlrev_b32_e32 v8, 16, v2
	v_and_b32_e32 v155, 0xffff0000, v2
	v_mul_f32_e32 v2, 0xbfb8aa3b, v6
	v_mul_f32_e32 v3, 0xbfb8aa3b, v7
	v_mul_f32_e32 v6, 0xbfb8aa3b, v158
	v_mul_f32_e32 v7, 0xbfb8aa3b, v159
	v_exp_f32_e32 v6, v6
	v_exp_f32_e32 v7, v7
	v_lshlrev_b32_e32 v4, 16, v0
	v_and_b32_e32 v5, 0xffff0000, v0
	v_mul_f32_e32 v0, 0xbfb8aa3b, v4
	v_pk_add_f32 v[6:7], v[6:7], 1.0 op_sel_hi:[1,0]
	v_mul_f32_e32 v4, 0xbfb8aa3b, v8
	v_div_scale_f32 v8, s[2:3], v7, v7, 1.0
	v_mul_f32_e32 v1, 0xbfb8aa3b, v5
	v_mul_f32_e32 v5, 0xbfb8aa3b, v155
	v_rcp_f32_e32 v155, v8
	v_exp_f32_e32 v4, v4
	v_exp_f32_e32 v5, v5
	v_exp_f32_e32 v2, v2
	v_fma_f32 v158, -v8, v155, 1.0
	v_fmac_f32_e32 v155, v158, v155
	v_div_scale_f32 v158, vcc, 1.0, v7, 1.0
	v_mul_f32_e32 v159, v158, v155
	v_fma_f32 v160, -v8, v159, v158
	v_fmac_f32_e32 v159, v160, v155
	v_fma_f32 v8, -v8, v159, v158
	v_div_fmas_f32 v8, v8, v155, v159
	v_div_fixup_f32 v7, v8, v7, 1.0
	v_div_scale_f32 v8, s[2:3], v6, v6, 1.0
	v_rcp_f32_e32 v155, v8
	v_pk_add_f32 v[4:5], v[4:5], 1.0 op_sel_hi:[1,0]
	v_exp_f32_e32 v3, v3
	v_exp_f32_e32 v0, v0
	v_fma_f32 v158, -v8, v155, 1.0
	v_fmac_f32_e32 v155, v158, v155
	v_div_scale_f32 v158, vcc, 1.0, v6, 1.0
	v_mul_f32_e32 v159, v158, v155
	v_fma_f32 v160, -v8, v159, v158
	v_fmac_f32_e32 v159, v160, v155
	v_fma_f32 v8, -v8, v159, v158
	v_div_fmas_f32 v8, v8, v155, v159
	v_div_fixup_f32 v6, v8, v6, 1.0
	v_div_scale_f32 v8, s[2:3], v5, v5, 1.0
	v_rcp_f32_e32 v155, v8
	v_pk_add_f32 v[2:3], v[2:3], 1.0 op_sel_hi:[1,0]
	v_exp_f32_e32 v1, v1
	v_fma_f32 v158, -v8, v155, 1.0
	v_fmac_f32_e32 v155, v158, v155
	v_div_scale_f32 v158, vcc, 1.0, v5, 1.0
	v_mul_f32_e32 v159, v158, v155
	v_fma_f32 v160, -v8, v159, v158
	v_fmac_f32_e32 v159, v160, v155
	v_fma_f32 v8, -v8, v159, v158
	v_div_fmas_f32 v8, v8, v155, v159
	v_div_fixup_f32 v5, v8, v5, 1.0
	v_div_scale_f32 v8, s[2:3], v4, v4, 1.0
	v_rcp_f32_e32 v155, v8
	v_pk_add_f32 v[0:1], v[0:1], 1.0 op_sel_hi:[1,0]
	v_fma_f32 v158, -v8, v155, 1.0
	v_fmac_f32_e32 v155, v158, v155
	v_div_scale_f32 v158, vcc, 1.0, v4, 1.0
	v_mul_f32_e32 v159, v158, v155
	v_fma_f32 v160, -v8, v159, v158
	v_fmac_f32_e32 v159, v160, v155
	v_fma_f32 v8, -v8, v159, v158
	v_div_fmas_f32 v8, v8, v155, v159
	v_div_fixup_f32 v4, v8, v4, 1.0
	v_div_scale_f32 v8, s[2:3], v3, v3, 1.0
	v_rcp_f32_e32 v155, v8
	s_nop 0
	v_fma_f32 v158, -v8, v155, 1.0
	v_fmac_f32_e32 v155, v158, v155
	v_div_scale_f32 v158, vcc, 1.0, v3, 1.0
	v_mul_f32_e32 v159, v158, v155
	v_fma_f32 v160, -v8, v159, v158
	v_fmac_f32_e32 v159, v160, v155
	v_fma_f32 v8, -v8, v159, v158
	v_div_fmas_f32 v8, v8, v155, v159
	v_div_fixup_f32 v3, v8, v3, 1.0
	v_div_scale_f32 v8, s[2:3], v2, v2, 1.0
	v_rcp_f32_e32 v155, v8
	s_nop 0
	v_fma_f32 v158, -v8, v155, 1.0
	v_fmac_f32_e32 v155, v158, v155
	v_div_scale_f32 v158, vcc, 1.0, v2, 1.0
	v_mul_f32_e32 v159, v158, v155
	v_fma_f32 v160, -v8, v159, v158
	v_fmac_f32_e32 v159, v160, v155
	v_fma_f32 v8, -v8, v159, v158
	v_div_fmas_f32 v8, v8, v155, v159
	v_div_fixup_f32 v2, v8, v2, 1.0
	v_div_scale_f32 v8, s[2:3], v1, v1, 1.0
	v_rcp_f32_e32 v155, v8
	s_nop 0
	v_fma_f32 v158, -v8, v155, 1.0
	v_fmac_f32_e32 v155, v158, v155
	v_div_scale_f32 v158, vcc, 1.0, v1, 1.0
	v_mul_f32_e32 v159, v158, v155
	v_fma_f32 v160, -v8, v159, v158
	v_fmac_f32_e32 v159, v160, v155
	v_fma_f32 v8, -v8, v159, v158
	v_div_fmas_f32 v8, v8, v155, v159
	v_div_fixup_f32 v1, v8, v1, 1.0
	v_div_scale_f32 v8, s[2:3], v0, v0, 1.0
	v_rcp_f32_e32 v155, v8
	s_nop 0
	v_fma_f32 v158, -v8, v155, 1.0
	v_fmac_f32_e32 v155, v158, v155
	v_div_scale_f32 v158, vcc, 1.0, v0, 1.0
	v_mul_f32_e32 v159, v158, v155
	v_fma_f32 v160, -v8, v159, v158
	v_fmac_f32_e32 v159, v160, v155
	v_fma_f32 v8, -v8, v159, v158
	v_div_fmas_f32 v8, v8, v155, v159
	v_div_fixup_f32 v0, v8, v0, 1.0
;     __device__ __forceinline__ void operator()(AccMut acc, const Unit& u, int wr, int wc, int, int) const {
;     ...
;                     if (u.seg < 2) {
;                         const v4u ga = *(const v4u*)(gp + u.seg * D), gb = *(const v4u*)(gp + (u.seg + 1) * D);
;                         const float la[8] = {bflo(ga.x), bfhi(ga.x), bflo(ga.y), bfhi(ga.y), bflo(ga.z), bfhi(ga.z), bflo(ga.w), bfhi(ga.w)};
;                         const float lb[8] = {bflo(gb.x), bfhi(gb.x), bflo(gb.y), bfhi(gb.y), bflo(gb.z), bfhi(gb.z), bflo(gb.w), bfhi(gb.w)};
; #pragma unroll
;                         for (int j = 0; j < 8; ++j) { const float ea = __expf(-fminf(fmaxf(la[j], -30.f), 30.f)), eb = __expf(-fminf(fmaxf(lb[j], -30.f), 30.f)); sc[j] = (1.0f + eb) * __builtin_amdgcn_rcpf(1.0f + ea); }
.LBB0_916:
	s_andn2_b64 vcc, exec, s[6:7]
	s_cbranch_vccnz .LBB0_918
	s_lshl_b32 s96, s50, 12
	v_lshl_add_u64 v[4:5], v[152:153], 0, s[96:97]
	global_load_dwordx4 v[0:3], v[4:5], off nt
	v_add_co_u32_e32 v4, vcc, 0x1000, v4
	s_nop 1
	v_addc_co_u32_e32 v5, vcc, 0, v5, vcc
	global_load_dwordx4 v[4:7], v[4:5], off nt
	s_waitcnt vmcnt(1)
	v_lshlrev_b32_e32 v8, 16, v0
	v_lshlrev_b32_e32 v152, 16, v1
	v_and_b32_e32 v0, 0xffff0000, v0
	v_and_b32_e32 v1, 0xffff0000, v1
	v_lshlrev_b32_e32 v153, 16, v2
	v_lshlrev_b32_e32 v155, 16, v3
	v_and_b32_e32 v165, 0xffff0000, v3
	v_max_f32_e32 v3, v8, v8
	v_max_f32_e32 v8, v152, v152
	v_max_f32_e32 v0, v0, v0
	v_max_f32_e32 v1, v1, v1
	v_max_f32_e32 v152, v153, v153
	v_max_f32_e32 v153, v155, v155
	v_med3_f32 v8, v8, s54, v223
	v_med3_f32 v3, v3, s54, v223
	v_med3_f32 v0, v0, s54, v223
	v_med3_f32 v1, v1, s54, v223
	v_med3_f32 v153, v153, s54, v223
	v_mul_f32_e32 v8, 0xbfb8aa3b, v8
	v_and_b32_e32 v2, 0xffff0000, v2
	v_mul_f32_e32 v3, 0xbfb8aa3b, v3
	v_mul_f32_e32 v0, 0xbfb8aa3b, v0
	v_mul_f32_e32 v1, 0xbfb8aa3b, v1
	v_mul_f32_e32 v153, 0xbfb8aa3b, v153
	v_exp_f32_e32 v8, v8
	v_max_f32_e32 v2, v2, v2
	v_exp_f32_e32 v161, v3
	v_exp_f32_e32 v164, v153
	v_med3_f32 v2, v2, s54, v223
	v_mul_f32_e32 v2, 0xbfb8aa3b, v2
	v_add_f32_e32 v8, 1.0, v8
	v_med3_f32 v152, v152, s54, v223
	v_mul_f32_e32 v152, 0xbfb8aa3b, v152
	v_exp_f32_e32 v152, v152
	s_waitcnt vmcnt(0)
	v_lshlrev_b32_e32 v155, 16, v4
	v_and_b32_e32 v4, 0xffff0000, v4
	v_lshlrev_b32_e32 v158, 16, v5
	v_max_f32_e32 v155, v155, v155
	v_max_f32_e32 v4, v4, v4
	v_max_f32_e32 v158, v158, v158
	v_and_b32_e32 v5, 0xffff0000, v5
	v_med3_f32 v3, v155, s54, v223
	v_exp_f32_e32 v155, v0
	v_med3_f32 v0, v4, s54, v223
	v_med3_f32 v4, v158, s54, v223
	v_exp_f32_e32 v158, v1
	v_lshlrev_b32_e32 v159, 16, v6
	v_and_b32_e32 v6, 0xffff0000, v6
	v_lshlrev_b32_e32 v160, 16, v7
	v_max_f32_e32 v5, v5, v5
	v_max_f32_e32 v159, v159, v159
	v_max_f32_e32 v6, v6, v6
	v_max_f32_e32 v160, v160, v160
	v_med3_f32 v1, v5, s54, v223
	v_med3_f32 v5, v159, s54, v223
	v_exp_f32_e32 v159, v2
	v_med3_f32 v2, v6, s54, v223
	v_med3_f32 v6, v160, s54, v223
	v_mul_f32_e32 v3, 0xbfb8aa3b, v3
	v_mul_f32_e32 v160, 0xbfb8aa3b, v1
	v_mul_f32_e32 v153, 0xbfb8aa3b, v0
	v_exp_f32_e32 v0, v3
	v_exp_f32_e32 v3, v160
	v_add_f32_e32 v160, 1.0, v158
	v_rcp_f32_e32 v158, v8
	v_add_f32_e32 v8, 1.0, v164
	v_rcp_f32_e32 v164, v8
	v_max_f32_e32 v8, v165, v165
	v_med3_f32 v8, v8, s54, v223
	v_mul_f32_e32 v8, 0xbfb8aa3b, v8
	v_and_b32_e32 v7, 0xffff0000, v7
	v_exp_f32_e32 v8, v8
	v_max_f32_e32 v7, v7, v7
	v_med3_f32 v7, v7, s54, v223
	v_mul_f32_e32 v4, 0xbfb8aa3b, v4
	v_mul_f32_e32 v5, 0xbfb8aa3b, v5
	v_mul_f32_e32 v166, 0xbfb8aa3b, v2
	v_mul_f32_e32 v6, 0xbfb8aa3b, v6
	v_mul_f32_e32 v7, 0xbfb8aa3b, v7
	v_exp_f32_e32 v1, v153
	v_exp_f32_e32 v2, v4
	v_exp_f32_e32 v4, v5
	v_exp_f32_e32 v5, v166
	v_add_f32_e32 v153, 1.0, v161
	v_add_f32_e32 v155, 1.0, v155
	v_add_f32_e32 v161, 1.0, v152
	v_add_f32_e32 v166, 1.0, v159
	v_exp_f32_e32 v6, v6
	v_exp_f32_e32 v7, v7
	v_add_f32_e32 v8, 1.0, v8
	v_rcp_f32_e32 v152, v153
	v_rcp_f32_e32 v153, v155
	v_rcp_f32_e32 v159, v160
	v_rcp_f32_e32 v160, v161
	v_rcp_f32_e32 v161, v166
	v_rcp_f32_e32 v165, v8
	v_pk_add_f32 v[0:1], v[0:1], 1.0 op_sel_hi:[1,0]
	v_pk_add_f32 v[2:3], v[2:3], 1.0 op_sel_hi:[1,0]
	v_pk_add_f32 v[4:5], v[4:5], 1.0 op_sel_hi:[1,0]
	v_pk_add_f32 v[6:7], v[6:7], 1.0 op_sel_hi:[1,0]
	v_pk_mul_f32 v[4:5], v[4:5], v[160:161]
	v_pk_mul_f32 v[6:7], v[6:7], v[164:165]
	v_pk_mul_f32 v[2:3], v[2:3], v[158:159]
	v_pk_mul_f32 v[0:1], v[0:1], v[152:153]

; __device__ __forceinline__ float sigmoidf_(float x) { return 1.0f / (1.0f + __expf(-x)); }
;     __device__ __forceinline__ void operator()(AccMut acc, const Unit& u, int wr, int wc, int, int) const {
;     ...
;                     const int row = row0 + ai * 128 + m * 16, col = col0 + bj * 128;
;                     const bf16* gp = PROJ + (size_t)row * DINP + GATE_OFF + col;
;                     float sc[8];
;                     if (u.seg < 2) {
;                         const v4u ga = *(const v4u*)(gp + u.seg * D), gb = *(const v4u*)(gp + (u.seg + 1) * D);
;                         const float la[8] = {bflo(ga.x), bfhi(ga.x), bflo(ga.y), bfhi(ga.y), bflo(ga.z), bfhi(ga.z), bflo(ga.w), bfhi(ga.w)};
;                         const float lb[8] = {bflo(gb.x), bfhi(gb.x), bflo(gb.y), bfhi(gb.y), bflo(gb.z), bfhi(gb.z), bflo(gb.w), bfhi(gb.w)};
; #pragma unroll
;                         for (int j = 0; j < 8; ++j) { const float ea = __expf(-fminf(fmaxf(la[j], -30.f), 30.f)), eb = __expf(-fminf(fmaxf(lb[j], -30.f), 30.f)); sc[j] = (1.0f + eb) * __builtin_amdgcn_rcpf(1.0f + ea); }
;                     } else {
;                         const v4u ga = *(const v4u*)(gp + 2 * D);
;                         const float la[8] = {bflo(ga.x), bfhi(ga.x), bflo(ga.y), bfhi(ga.y), bflo(ga.z), bfhi(ga.z), bflo(ga.w), bfhi(ga.w)};
; #pragma unroll
;                         for (int j = 0; j < 8; ++j) sc[j] = sigmoidf_(la[j]);
.LBB0_921:
	v_add_u32_e32 v152, 0x80, v150
	v_cndmask_b32_e64 v0, 0, 1, s[22:23]
	v_ashrrev_i32_e32 v153, 31, v152
	v_cmp_ne_u32_e64 s[6:7], 1, v0
	s_andn2_b64 vcc, exec, s[22:23]
	s_mov_b64 s[2:3], -1
	s_cbranch_vccnz .LBB0_923
	v_lshl_add_u64 v[0:1], v[152:153], 1, v[156:157]
	v_add_co_u32_e32 v0, vcc, 0x2000, v0
	s_nop 1
	v_addc_co_u32_e32 v1, vcc, 0, v1, vcc
	global_load_dwordx4 v[0:3], v[0:1], off nt
	s_waitcnt vmcnt(0)
	v_lshlrev_b32_e32 v6, 16, v1
	v_and_b32_e32 v7, 0xffff0000, v1
	v_lshlrev_b32_e32 v160, 16, v3
	v_and_b32_e32 v161, 0xffff0000, v3
	v_lshlrev_b32_e32 v8, 16, v2
	v_and_b32_e32 v155, 0xffff0000, v2
	v_mul_f32_e32 v2, 0xbfb8aa3b, v6
	v_mul_f32_e32 v3, 0xbfb8aa3b, v7
	v_mul_f32_e32 v6, 0xbfb8aa3b, v160
	v_mul_f32_e32 v7, 0xbfb8aa3b, v161
	v_exp_f32_e32 v6, v6
	v_exp_f32_e32 v7, v7
	v_lshlrev_b32_e32 v4, 16, v0
	v_and_b32_e32 v5, 0xffff0000, v0
	v_mul_f32_e32 v0, 0xbfb8aa3b, v4
	v_pk_add_f32 v[6:7], v[6:7], 1.0 op_sel_hi:[1,0]
	v_mul_f32_e32 v4, 0xbfb8aa3b, v8
	v_div_scale_f32 v8, s[2:3], v7, v7, 1.0
	v_mul_f32_e32 v1, 0xbfb8aa3b, v5
	v_mul_f32_e32 v5, 0xbfb8aa3b, v155
	v_rcp_f32_e32 v155, v8
	v_exp_f32_e32 v4, v4
	v_exp_f32_e32 v5, v5
	v_exp_f32_e32 v2, v2
	v_fma_f32 v160, -v8, v155, 1.0
	v_fmac_f32_e32 v155, v160, v155
	v_div_scale_f32 v160, vcc, 1.0, v7, 1.0
	v_mul_f32_e32 v161, v160, v155
	v_fma_f32 v164, -v8, v161, v160
	v_fmac_f32_e32 v161, v164, v155
	v_fma_f32 v8, -v8, v161, v160
	v_div_fmas_f32 v8, v8, v155, v161
	v_div_fixup_f32 v7, v8, v7, 1.0
	v_div_scale_f32 v8, s[2:3], v6, v6, 1.0
	v_rcp_f32_e32 v155, v8
	v_pk_add_f32 v[4:5], v[4:5], 1.0 op_sel_hi:[1,0]
	v_exp_f32_e32 v3, v3
	v_exp_f32_e32 v0, v0
	v_fma_f32 v160, -v8, v155, 1.0
	v_fmac_f32_e32 v155, v160, v155
	v_div_scale_f32 v160, vcc, 1.0, v6, 1.0
	v_mul_f32_e32 v161, v160, v155
	v_fma_f32 v164, -v8, v161, v160
	v_fmac_f32_e32 v161, v164, v155
	v_fma_f32 v8, -v8, v161, v160
	v_div_fmas_f32 v8, v8, v155, v161
	v_div_fixup_f32 v6, v8, v6, 1.0
	v_div_scale_f32 v8, s[2:3], v5, v5, 1.0
	v_rcp_f32_e32 v155, v8
	v_pk_add_f32 v[2:3], v[2:3], 1.0 op_sel_hi:[1,0]
	v_exp_f32_e32 v1, v1
	v_fma_f32 v160, -v8, v155, 1.0
	v_fmac_f32_e32 v155, v160, v155
	v_div_scale_f32 v160, vcc, 1.0, v5, 1.0
	v_mul_f32_e32 v161, v160, v155
	v_fma_f32 v164, -v8, v161, v160
	v_fmac_f32_e32 v161, v164, v155
	v_fma_f32 v8, -v8, v161, v160
	v_div_fmas_f32 v8, v8, v155, v161
	v_div_fixup_f32 v5, v8, v5, 1.0
	v_div_scale_f32 v8, s[2:3], v4, v4, 1.0
	v_rcp_f32_e32 v155, v8
	v_pk_add_f32 v[0:1], v[0:1], 1.0 op_sel_hi:[1,0]
	v_fma_f32 v160, -v8, v155, 1.0
	v_fmac_f32_e32 v155, v160, v155
	v_div_scale_f32 v160, vcc, 1.0, v4, 1.0
	v_mul_f32_e32 v161, v160, v155
	v_fma_f32 v164, -v8, v161, v160
	v_fmac_f32_e32 v161, v164, v155
	v_fma_f32 v8, -v8, v161, v160
	v_div_fmas_f32 v8, v8, v155, v161
	v_div_fixup_f32 v4, v8, v4, 1.0
	v_div_scale_f32 v8, s[2:3], v3, v3, 1.0
	v_rcp_f32_e32 v155, v8
	s_nop 0
	v_fma_f32 v160, -v8, v155, 1.0
	v_fmac_f32_e32 v155, v160, v155
	v_div_scale_f32 v160, vcc, 1.0, v3, 1.0
	v_mul_f32_e32 v161, v160, v155
	v_fma_f32 v164, -v8, v161, v160
	v_fmac_f32_e32 v161, v164, v155
	v_fma_f32 v8, -v8, v161, v160
	v_div_fmas_f32 v8, v8, v155, v161
	v_div_fixup_f32 v3, v8, v3, 1.0
	v_div_scale_f32 v8, s[2:3], v2, v2, 1.0
	v_rcp_f32_e32 v155, v8
	s_nop 0
	v_fma_f32 v160, -v8, v155, 1.0
	v_fmac_f32_e32 v155, v160, v155
	v_div_scale_f32 v160, vcc, 1.0, v2, 1.0
	v_mul_f32_e32 v161, v160, v155
	v_fma_f32 v164, -v8, v161, v160
	v_fmac_f32_e32 v161, v164, v155
	v_fma_f32 v8, -v8, v161, v160
	v_div_fmas_f32 v8, v8, v155, v161
	v_div_fixup_f32 v2, v8, v2, 1.0
	v_div_scale_f32 v8, s[2:3], v1, v1, 1.0
	v_rcp_f32_e32 v155, v8
	s_nop 0
	v_fma_f32 v160, -v8, v155, 1.0
	v_fmac_f32_e32 v155, v160, v155
	v_div_scale_f32 v160, vcc, 1.0, v1, 1.0
	v_mul_f32_e32 v161, v160, v155
	v_fma_f32 v164, -v8, v161, v160
	v_fmac_f32_e32 v161, v164, v155
	v_fma_f32 v8, -v8, v161, v160
	v_div_fmas_f32 v8, v8, v155, v161
	v_div_fixup_f32 v1, v8, v1, 1.0
	v_div_scale_f32 v8, s[2:3], v0, v0, 1.0
	v_rcp_f32_e32 v155, v8
	s_mov_b64 s[2:3], 0
	v_fma_f32 v160, -v8, v155, 1.0
	v_fmac_f32_e32 v155, v160, v155
	v_div_scale_f32 v160, vcc, 1.0, v0, 1.0
	v_mul_f32_e32 v161, v160, v155
	v_fma_f32 v164, -v8, v161, v160
	v_fmac_f32_e32 v161, v164, v155
	v_fma_f32 v8, -v8, v161, v160
	v_div_fmas_f32 v8, v8, v155, v161
	v_div_fixup_f32 v0, v8, v0, 1.0
;     __device__ __forceinline__ void operator()(AccMut acc, const Unit& u, int wr, int wc, int, int) const {
;     ...
;                     if (u.seg < 2) {
;                         const v4u ga = *(const v4u*)(gp + u.seg * D), gb = *(const v4u*)(gp + (u.seg + 1) * D);
;                         const float la[8] = {bflo(ga.x), bfhi(ga.x), bflo(ga.y), bfhi(ga.y), bflo(ga.z), bfhi(ga.z), bflo(ga.w), bfhi(ga.w)};
;                         const float lb[8] = {bflo(gb.x), bfhi(gb.x), bflo(gb.y), bfhi(gb.y), bflo(gb.z), bfhi(gb.z), bflo(gb.w), bfhi(gb.w)};
; #pragma unroll
;                         for (int j = 0; j < 8; ++j) { const float ea = __expf(-fminf(fmaxf(la[j], -30.f), 30.f)), eb = __expf(-fminf(fmaxf(lb[j], -30.f), 30.f)); sc[j] = (1.0f + eb) * __builtin_amdgcn_rcpf(1.0f + ea); }
.LBB0_923:
	s_andn2_b64 vcc, exec, s[2:3]
	s_cbranch_vccnz .LBB0_925
	s_lshl_b32 s96, s50, 12
	v_lshl_add_u64 v[0:1], v[156:157], 0, s[96:97]
	v_lshl_add_u64 v[4:5], v[152:153], 1, v[0:1]
	global_load_dwordx4 v[0:3], v[4:5], off nt
	v_add_co_u32_e32 v4, vcc, 0x1000, v4
	s_nop 1
	v_addc_co_u32_e32 v5, vcc, 0, v5, vcc
	global_load_dwordx4 v[4:7], v[4:5], off nt
	s_waitcnt vmcnt(1)
	v_lshlrev_b32_e32 v8, 16, v0
	v_lshlrev_b32_e32 v155, 16, v1
	v_and_b32_e32 v0, 0xffff0000, v0
	v_and_b32_e32 v1, 0xffff0000, v1
	v_lshlrev_b32_e32 v156, 16, v2
	v_lshlrev_b32_e32 v157, 16, v3
	v_and_b32_e32 v167, 0xffff0000, v3
	v_max_f32_e32 v3, v8, v8
	v_max_f32_e32 v8, v155, v155
	v_max_f32_e32 v0, v0, v0
	v_max_f32_e32 v1, v1, v1
	v_max_f32_e32 v155, v156, v156
	v_max_f32_e32 v156, v157, v157
	v_med3_f32 v8, v8, s54, v223
	v_med3_f32 v3, v3, s54, v223
	v_med3_f32 v0, v0, s54, v223
	v_med3_f32 v1, v1, s54, v223
	v_med3_f32 v156, v156, s54, v223
	v_mul_f32_e32 v8, 0xbfb8aa3b, v8
	v_and_b32_e32 v2, 0xffff0000, v2
	v_mul_f32_e32 v3, 0xbfb8aa3b, v3
	v_mul_f32_e32 v0, 0xbfb8aa3b, v0
	v_mul_f32_e32 v1, 0xbfb8aa3b, v1
	v_mul_f32_e32 v156, 0xbfb8aa3b, v156
	v_exp_f32_e32 v8, v8
	v_max_f32_e32 v2, v2, v2
	v_exp_f32_e32 v165, v3
	v_exp_f32_e32 v166, v156
	v_med3_f32 v2, v2, s54, v223
	v_mul_f32_e32 v2, 0xbfb8aa3b, v2
	v_add_f32_e32 v8, 1.0, v8
	v_med3_f32 v155, v155, s54, v223
	v_mul_f32_e32 v155, 0xbfb8aa3b, v155
	v_exp_f32_e32 v155, v155
	s_waitcnt vmcnt(0)
	v_lshlrev_b32_e32 v157, 16, v4
	v_and_b32_e32 v4, 0xffff0000, v4
	v_lshlrev_b32_e32 v160, 16, v5
	v_max_f32_e32 v157, v157, v157
	v_max_f32_e32 v4, v4, v4
	v_max_f32_e32 v160, v160, v160
	v_and_b32_e32 v5, 0xffff0000, v5
	v_med3_f32 v3, v157, s54, v223
	v_exp_f32_e32 v157, v0
	v_med3_f32 v0, v4, s54, v223
	v_med3_f32 v4, v160, s54, v223
	v_exp_f32_e32 v160, v1
	v_lshlrev_b32_e32 v161, 16, v6
	v_and_b32_e32 v6, 0xffff0000, v6
	v_lshlrev_b32_e32 v164, 16, v7
	v_max_f32_e32 v5, v5, v5
	v_max_f32_e32 v161, v161, v161
	v_max_f32_e32 v6, v6, v6
	v_max_f32_e32 v164, v164, v164
	v_med3_f32 v1, v5, s54, v223
	v_med3_f32 v5, v161, s54, v223
	v_exp_f32_e32 v161, v2
	v_med3_f32 v2, v6, s54, v223
	v_med3_f32 v6, v164, s54, v223
	v_mul_f32_e32 v3, 0xbfb8aa3b, v3
	v_mul_f32_e32 v164, 0xbfb8aa3b, v1
	v_mul_f32_e32 v156, 0xbfb8aa3b, v0
	v_exp_f32_e32 v0, v3
	v_exp_f32_e32 v3, v164
	v_add_f32_e32 v164, 1.0, v160
	v_rcp_f32_e32 v160, v8
	v_add_f32_e32 v8, 1.0, v166
	v_rcp_f32_e32 v166, v8
	v_max_f32_e32 v8, v167, v167
	v_med3_f32 v8, v8, s54, v223
	v_mul_f32_e32 v8, 0xbfb8aa3b, v8
	v_and_b32_e32 v7, 0xffff0000, v7
	v_exp_f32_e32 v8, v8
	v_max_f32_e32 v7, v7, v7
	v_med3_f32 v7, v7, s54, v223
	v_mul_f32_e32 v4, 0xbfb8aa3b, v4
	v_mul_f32_e32 v5, 0xbfb8aa3b, v5
	v_mul_f32_e32 v168, 0xbfb8aa3b, v2
	v_mul_f32_e32 v6, 0xbfb8aa3b, v6
	v_mul_f32_e32 v7, 0xbfb8aa3b, v7
	v_exp_f32_e32 v1, v156
	v_exp_f32_e32 v2, v4
	v_exp_f32_e32 v4, v5
	v_exp_f32_e32 v5, v168
	v_add_f32_e32 v156, 1.0, v165
	v_add_f32_e32 v157, 1.0, v157
	v_add_f32_e32 v155, 1.0, v155
	v_add_f32_e32 v165, 1.0, v161
	v_exp_f32_e32 v6, v6
	v_exp_f32_e32 v7, v7
	v_add_f32_e32 v8, 1.0, v8
	v_rcp_f32_e32 v156, v156
	v_rcp_f32_e32 v157, v157
	v_rcp_f32_e32 v161, v164
	v_rcp_f32_e32 v164, v155
	v_rcp_f32_e32 v165, v165
	v_rcp_f32_e32 v167, v8
	v_pk_add_f32 v[0:1], v[0:1], 1.0 op_sel_hi:[1,0]
	v_pk_add_f32 v[2:3], v[2:3], 1.0 op_sel_hi:[1,0]
	v_pk_add_f32 v[4:5], v[4:5], 1.0 op_sel_hi:[1,0]
	v_pk_add_f32 v[6:7], v[6:7], 1.0 op_sel_hi:[1,0]
	v_pk_mul_f32 v[4:5], v[4:5], v[164:165]
	v_pk_mul_f32 v[6:7], v[6:7], v[166:167]
	v_pk_mul_f32 v[2:3], v[2:3], v[160:161]
	v_pk_mul_f32 v[0:1], v[0:1], v[156:157]

; __device__ __forceinline__ float sigmoidf_(float x) { return 1.0f / (1.0f + __expf(-x)); }
;     __device__ __forceinline__ void operator()(AccMut acc, const Unit& u, int wr, int wc, int, int) const {
;     ...
;                     const int row = row0 + ai * 128 + m * 16, col = col0 + bj * 128;
;                     const bf16* gp = PROJ + (size_t)row * DINP + GATE_OFF + col;
;                     float sc[8];
;                     if (u.seg < 2) {
;                         const v4u ga = *(const v4u*)(gp + u.seg * D), gb = *(const v4u*)(gp + (u.seg + 1) * D);
;                         const float la[8] = {bflo(ga.x), bfhi(ga.x), bflo(ga.y), bfhi(ga.y), bflo(ga.z), bfhi(ga.z), bflo(ga.w), bfhi(ga.w)};
;                         const float lb[8] = {bflo(gb.x), bfhi(gb.x), bflo(gb.y), bfhi(gb.y), bflo(gb.z), bfhi(gb.z), bflo(gb.w), bfhi(gb.w)};
; #pragma unroll
;                         for (int j = 0; j < 8; ++j) { const float ea = __expf(-fminf(fmaxf(la[j], -30.f), 30.f)), eb = __expf(-fminf(fmaxf(lb[j], -30.f), 30.f)); sc[j] = (1.0f + eb) * __builtin_amdgcn_rcpf(1.0f + ea); }
;                     } else {
;                         const v4u ga = *(const v4u*)(gp + 2 * D);
;                         const float la[8] = {bflo(ga.x), bfhi(ga.x), bflo(ga.y), bfhi(ga.y), bflo(ga.z), bfhi(ga.z), bflo(ga.w), bfhi(ga.w)};
; #pragma unroll
;                         for (int j = 0; j < 8; ++j) sc[j] = sigmoidf_(la[j]);
.LBB0_928:
	v_or_b32_e32 v158, 16, v154
	v_mov_b64_e32 v[0:1], s[8:9]
	v_mad_i64_i32 v[0:1], s[2:3], v158, s91, v[0:1]
	s_andn2_b64 vcc, exec, s[22:23]
	v_lshl_add_u64 v[156:157], v[0:1], 0, s[56:57]
	v_lshl_add_u64 v[160:161], v[150:151], 1, v[156:157]
	s_and_b64 vcc, exec, s[6:7]
	s_mov_b64 s[2:3], -1
	s_cbranch_vccnz .LBB0_930
	v_add_co_u32_e32 v0, vcc, 0x2000, v160
	s_nop 1
	v_addc_co_u32_e32 v1, vcc, 0, v161, vcc
	global_load_dwordx4 v[0:3], v[0:1], off nt
	s_waitcnt vmcnt(0)
	v_lshlrev_b32_e32 v6, 16, v1
	v_and_b32_e32 v7, 0xffff0000, v1
	v_lshlrev_b32_e32 v159, 16, v3
	v_and_b32_e32 v164, 0xffff0000, v3
	v_lshlrev_b32_e32 v8, 16, v2
	v_and_b32_e32 v155, 0xffff0000, v2
	v_mul_f32_e32 v2, 0xbfb8aa3b, v6
	v_mul_f32_e32 v3, 0xbfb8aa3b, v7
	v_mul_f32_e32 v6, 0xbfb8aa3b, v159
	v_mul_f32_e32 v7, 0xbfb8aa3b, v164
	v_exp_f32_e32 v6, v6
	v_exp_f32_e32 v7, v7
	v_lshlrev_b32_e32 v4, 16, v0
	v_and_b32_e32 v5, 0xffff0000, v0
	v_mul_f32_e32 v0, 0xbfb8aa3b, v4
	v_pk_add_f32 v[6:7], v[6:7], 1.0 op_sel_hi:[1,0]
	v_mul_f32_e32 v4, 0xbfb8aa3b, v8
	v_div_scale_f32 v8, s[2:3], v7, v7, 1.0
	v_mul_f32_e32 v1, 0xbfb8aa3b, v5
	v_mul_f32_e32 v5, 0xbfb8aa3b, v155
	v_rcp_f32_e32 v155, v8
	v_exp_f32_e32 v4, v4
	v_exp_f32_e32 v5, v5
	v_exp_f32_e32 v2, v2
	v_fma_f32 v159, -v8, v155, 1.0
	v_fmac_f32_e32 v155, v159, v155
	v_div_scale_f32 v159, vcc, 1.0, v7, 1.0
	v_mul_f32_e32 v164, v159, v155
	v_fma_f32 v165, -v8, v164, v159
	v_fmac_f32_e32 v164, v165, v155
	v_fma_f32 v8, -v8, v164, v159
	v_div_fmas_f32 v8, v8, v155, v164
	v_div_fixup_f32 v7, v8, v7, 1.0
	v_div_scale_f32 v8, s[2:3], v6, v6, 1.0
	v_rcp_f32_e32 v155, v8
	v_pk_add_f32 v[4:5], v[4:5], 1.0 op_sel_hi:[1,0]
	v_exp_f32_e32 v3, v3
	v_exp_f32_e32 v0, v0
	v_fma_f32 v159, -v8, v155, 1.0
	v_fmac_f32_e32 v155, v159, v155
	v_div_scale_f32 v159, vcc, 1.0, v6, 1.0
	v_mul_f32_e32 v164, v159, v155
	v_fma_f32 v165, -v8, v164, v159
	v_fmac_f32_e32 v164, v165, v155
	v_fma_f32 v8, -v8, v164, v159
	v_div_fmas_f32 v8, v8, v155, v164
	v_div_fixup_f32 v6, v8, v6, 1.0
	v_div_scale_f32 v8, s[2:3], v5, v5, 1.0
	v_rcp_f32_e32 v155, v8
	v_pk_add_f32 v[2:3], v[2:3], 1.0 op_sel_hi:[1,0]
	v_exp_f32_e32 v1, v1
	v_fma_f32 v159, -v8, v155, 1.0
	v_fmac_f32_e32 v155, v159, v155
	v_div_scale_f32 v159, vcc, 1.0, v5, 1.0
	v_mul_f32_e32 v164, v159, v155
	v_fma_f32 v165, -v8, v164, v159
	v_fmac_f32_e32 v164, v165, v155
	v_fma_f32 v8, -v8, v164, v159
	v_div_fmas_f32 v8, v8, v155, v164
	v_div_fixup_f32 v5, v8, v5, 1.0
	v_div_scale_f32 v8, s[2:3], v4, v4, 1.0
	v_rcp_f32_e32 v155, v8
	v_pk_add_f32 v[0:1], v[0:1], 1.0 op_sel_hi:[1,0]
	v_fma_f32 v159, -v8, v155, 1.0
	v_fmac_f32_e32 v155, v159, v155
	v_div_scale_f32 v159, vcc, 1.0, v4, 1.0
	v_mul_f32_e32 v164, v159, v155
	v_fma_f32 v165, -v8, v164, v159
	v_fmac_f32_e32 v164, v165, v155
	v_fma_f32 v8, -v8, v164, v159
	v_div_fmas_f32 v8, v8, v155, v164
	v_div_fixup_f32 v4, v8, v4, 1.0
	v_div_scale_f32 v8, s[2:3], v3, v3, 1.0
	v_rcp_f32_e32 v155, v8
	s_nop 0
	v_fma_f32 v159, -v8, v155, 1.0
	v_fmac_f32_e32 v155, v159, v155
	v_div_scale_f32 v159, vcc, 1.0, v3, 1.0
	v_mul_f32_e32 v164, v159, v155
	v_fma_f32 v165, -v8, v164, v159
	v_fmac_f32_e32 v164, v165, v155
	v_fma_f32 v8, -v8, v164, v159
	v_div_fmas_f32 v8, v8, v155, v164
	v_div_fixup_f32 v3, v8, v3, 1.0
	v_div_scale_f32 v8, s[2:3], v2, v2, 1.0
	v_rcp_f32_e32 v155, v8
	s_nop 0
	v_fma_f32 v159, -v8, v155, 1.0
	v_fmac_f32_e32 v155, v159, v155
	v_div_scale_f32 v159, vcc, 1.0, v2, 1.0
	v_mul_f32_e32 v164, v159, v155
	v_fma_f32 v165, -v8, v164, v159
	v_fmac_f32_e32 v164, v165, v155
	v_fma_f32 v8, -v8, v164, v159
	v_div_fmas_f32 v8, v8, v155, v164
	v_div_fixup_f32 v2, v8, v2, 1.0
	v_div_scale_f32 v8, s[2:3], v1, v1, 1.0
	v_rcp_f32_e32 v155, v8
	s_nop 0
	v_fma_f32 v159, -v8, v155, 1.0
	v_fmac_f32_e32 v155, v159, v155
	v_div_scale_f32 v159, vcc, 1.0, v1, 1.0
	v_mul_f32_e32 v164, v159, v155
	v_fma_f32 v165, -v8, v164, v159
	v_fmac_f32_e32 v164, v165, v155
	v_fma_f32 v8, -v8, v164, v159
	v_div_fmas_f32 v8, v8, v155, v164
	v_div_fixup_f32 v1, v8, v1, 1.0
	v_div_scale_f32 v8, s[2:3], v0, v0, 1.0
	v_rcp_f32_e32 v155, v8
	s_mov_b64 s[2:3], 0
	v_fma_f32 v159, -v8, v155, 1.0
	v_fmac_f32_e32 v155, v159, v155
	v_div_scale_f32 v159, vcc, 1.0, v0, 1.0
	v_mul_f32_e32 v164, v159, v155
	v_fma_f32 v165, -v8, v164, v159
	v_fmac_f32_e32 v164, v165, v155
	v_fma_f32 v8, -v8, v164, v159
	v_div_fmas_f32 v8, v8, v155, v164
	v_div_fixup_f32 v0, v8, v0, 1.0
;     __device__ __forceinline__ void operator()(AccMut acc, const Unit& u, int wr, int wc, int, int) const {
;     ...
;                     if (u.seg < 2) {
;                         const v4u ga = *(const v4u*)(gp + u.seg * D), gb = *(const v4u*)(gp + (u.seg + 1) * D);
;                         const float la[8] = {bflo(ga.x), bfhi(ga.x), bflo(ga.y), bfhi(ga.y), bflo(ga.z), bfhi(ga.z), bflo(ga.w), bfhi(ga.w)};
;                         const float lb[8] = {bflo(gb.x), bfhi(gb.x), bflo(gb.y), bfhi(gb.y), bflo(gb.z), bfhi(gb.z), bflo(gb.w), bfhi(gb.w)};
; #pragma unroll
;                         for (int j = 0; j < 8; ++j) { const float ea = __expf(-fminf(fmaxf(la[j], -30.f), 30.f)), eb = __expf(-fminf(fmaxf(lb[j], -30.f), 30.f)); sc[j] = (1.0f + eb) * __builtin_amdgcn_rcpf(1.0f + ea); }
.LBB0_930:
	s_andn2_b64 vcc, exec, s[2:3]
	s_cbranch_vccnz .LBB0_932
	s_lshl_b32 s96, s50, 12
	v_lshl_add_u64 v[4:5], v[160:161], 0, s[96:97]
	global_load_dwordx4 v[0:3], v[4:5], off nt
	v_add_co_u32_e32 v4, vcc, 0x1000, v4
	s_nop 1
	v_addc_co_u32_e32 v5, vcc, 0, v5, vcc
	global_load_dwordx4 v[4:7], v[4:5], off nt
	s_waitcnt vmcnt(1)
	v_lshlrev_b32_e32 v8, 16, v0
	v_lshlrev_b32_e32 v155, 16, v1
	v_and_b32_e32 v0, 0xffff0000, v0
	v_and_b32_e32 v1, 0xffff0000, v1
	v_lshlrev_b32_e32 v159, 16, v2
	v_and_b32_e32 v2, 0xffff0000, v2
	v_lshlrev_b32_e32 v160, 16, v3
	v_and_b32_e32 v169, 0xffff0000, v3
	v_max_f32_e32 v3, v8, v8
	v_max_f32_e32 v8, v155, v155
	v_max_f32_e32 v0, v0, v0
	v_max_f32_e32 v1, v1, v1
	v_max_f32_e32 v155, v159, v159
	v_max_f32_e32 v2, v2, v2
	v_max_f32_e32 v159, v160, v160
	v_med3_f32 v8, v8, s54, v223
	v_med3_f32 v3, v3, s54, v223
	v_med3_f32 v0, v0, s54, v223
	v_med3_f32 v1, v1, s54, v223
	v_med3_f32 v2, v2, s54, v223
	v_med3_f32 v159, v159, s54, v223
	v_mul_f32_e32 v8, 0xbfb8aa3b, v8
	v_mul_f32_e32 v3, 0xbfb8aa3b, v3
	v_mul_f32_e32 v0, 0xbfb8aa3b, v0
	v_mul_f32_e32 v1, 0xbfb8aa3b, v1
	v_mul_f32_e32 v2, 0xbfb8aa3b, v2
	v_mul_f32_e32 v159, 0xbfb8aa3b, v159
	v_exp_f32_e32 v8, v8
	v_exp_f32_e32 v166, v3
	v_exp_f32_e32 v159, v159
	v_med3_f32 v155, v155, s54, v223
	v_add_f32_e32 v8, 1.0, v8
	v_mul_f32_e32 v155, 0xbfb8aa3b, v155
	v_exp_f32_e32 v155, v155
	s_waitcnt vmcnt(0)
	v_lshlrev_b32_e32 v160, 16, v4
	v_and_b32_e32 v4, 0xffff0000, v4
	v_lshlrev_b32_e32 v161, 16, v5
	v_and_b32_e32 v5, 0xffff0000, v5
	v_lshlrev_b32_e32 v164, 16, v6
	v_max_f32_e32 v160, v160, v160
	v_max_f32_e32 v4, v4, v4
	v_max_f32_e32 v161, v161, v161
	v_max_f32_e32 v5, v5, v5
	v_max_f32_e32 v164, v164, v164
	v_and_b32_e32 v6, 0xffff0000, v6
	v_med3_f32 v3, v160, s54, v223
	v_exp_f32_e32 v160, v0
	v_med3_f32 v0, v4, s54, v223
	v_med3_f32 v4, v161, s54, v223
	v_exp_f32_e32 v161, v1
	v_med3_f32 v1, v5, s54, v223
	v_med3_f32 v5, v164, s54, v223
	v_exp_f32_e32 v164, v2
	v_lshlrev_b32_e32 v165, 16, v7
	v_max_f32_e32 v6, v6, v6
	v_max_f32_e32 v165, v165, v165
	v_med3_f32 v2, v6, s54, v223
	v_med3_f32 v6, v165, s54, v223
	v_mul_f32_e32 v3, 0xbfb8aa3b, v3
	v_mul_f32_e32 v165, 0xbfb8aa3b, v0
	v_mul_f32_e32 v4, 0xbfb8aa3b, v4
	v_mul_f32_e32 v167, 0xbfb8aa3b, v1
	v_mul_f32_e32 v5, 0xbfb8aa3b, v5
	v_mul_f32_e32 v168, 0xbfb8aa3b, v2
	v_exp_f32_e32 v0, v3
	v_exp_f32_e32 v1, v165
	v_exp_f32_e32 v2, v4
	v_exp_f32_e32 v3, v167
	v_exp_f32_e32 v4, v5
	v_exp_f32_e32 v5, v168
	v_add_f32_e32 v165, 1.0, v166
	v_add_f32_e32 v167, 1.0, v161
	v_add_f32_e32 v168, 1.0, v164
	v_rcp_f32_e32 v164, v8
	v_add_f32_e32 v8, 1.0, v159
	v_add_f32_e32 v166, 1.0, v160
	v_rcp_f32_e32 v160, v165
	v_rcp_f32_e32 v165, v167
	v_rcp_f32_e32 v167, v168
	v_rcp_f32_e32 v168, v8
	v_max_f32_e32 v8, v169, v169
	v_med3_f32 v8, v8, s54, v223
	v_mul_f32_e32 v8, 0xbfb8aa3b, v8
	v_and_b32_e32 v7, 0xffff0000, v7
	v_exp_f32_e32 v8, v8
	v_max_f32_e32 v7, v7, v7
	v_med3_f32 v7, v7, s54, v223
	v_mul_f32_e32 v6, 0xbfb8aa3b, v6
	v_mul_f32_e32 v7, 0xbfb8aa3b, v7
	v_add_f32_e32 v155, 1.0, v155
	v_exp_f32_e32 v6, v6
	v_exp_f32_e32 v7, v7
	v_add_f32_e32 v8, 1.0, v8
	v_rcp_f32_e32 v161, v166
	v_rcp_f32_e32 v166, v155
	v_rcp_f32_e32 v169, v8
	v_pk_add_f32 v[0:1], v[0:1], 1.0 op_sel_hi:[1,0]
	v_pk_add_f32 v[2:3], v[2:3], 1.0 op_sel_hi:[1,0]
	v_pk_add_f32 v[4:5], v[4:5], 1.0 op_sel_hi:[1,0]
	v_pk_add_f32 v[6:7], v[6:7], 1.0 op_sel_hi:[1,0]
	v_pk_mul_f32 v[4:5], v[4:5], v[166:167]
	v_pk_mul_f32 v[6:7], v[6:7], v[168:169]
	v_pk_mul_f32 v[2:3], v[2:3], v[164:165]
	v_pk_mul_f32 v[0:1], v[0:1], v[160:161]

; __device__ __forceinline__ float sigmoidf_(float x) { return 1.0f / (1.0f + __expf(-x)); }
;     __device__ __forceinline__ void operator()(AccMut acc, const Unit& u, int wr, int wc, int, int) const {
;     ...
;                     const int row = row0 + ai * 128 + m * 16, col = col0 + bj * 128;
;                     const bf16* gp = PROJ + (size_t)row * DINP + GATE_OFF + col;
;                     float sc[8];
;                     if (u.seg < 2) {
;                         const v4u ga = *(const v4u*)(gp + u.seg * D), gb = *(const v4u*)(gp + (u.seg + 1) * D);
;                         const float la[8] = {bflo(ga.x), bfhi(ga.x), bflo(ga.y), bfhi(ga.y), bflo(ga.z), bfhi(ga.z), bflo(ga.w), bfhi(ga.w)};
;                         const float lb[8] = {bflo(gb.x), bfhi(gb.x), bflo(gb.y), bfhi(gb.y), bflo(gb.z), bfhi(gb.z), bflo(gb.w), bfhi(gb.w)};
; #pragma unroll
;                         for (int j = 0; j < 8; ++j) { const float ea = __expf(-fminf(fmaxf(la[j], -30.f), 30.f)), eb = __expf(-fminf(fmaxf(lb[j], -30.f), 30.f)); sc[j] = (1.0f + eb) * __builtin_amdgcn_rcpf(1.0f + ea); }
;                     } else {
;                         const v4u ga = *(const v4u*)(gp + 2 * D);
;                         const float la[8] = {bflo(ga.x), bfhi(ga.x), bflo(ga.y), bfhi(ga.y), bflo(ga.z), bfhi(ga.z), bflo(ga.w), bfhi(ga.w)};
; #pragma unroll
;                         for (int j = 0; j < 8; ++j) sc[j] = sigmoidf_(la[j]);
.LBB0_935:
	v_lshl_add_u64 v[0:1], v[152:153], 1, v[156:157]
	v_add_co_u32_e32 v0, vcc, 0x2000, v0
	s_nop 1
	v_addc_co_u32_e32 v1, vcc, 0, v1, vcc
	global_load_dwordx4 v[0:3], v[0:1], off nt
	s_waitcnt vmcnt(0)
	v_lshlrev_b32_e32 v6, 16, v1
	v_and_b32_e32 v7, 0xffff0000, v1
	v_lshlrev_b32_e32 v160, 16, v3
	v_and_b32_e32 v161, 0xffff0000, v3
	v_lshlrev_b32_e32 v8, 16, v2
	v_and_b32_e32 v155, 0xffff0000, v2
	v_mul_f32_e32 v2, 0xbfb8aa3b, v6
	v_mul_f32_e32 v3, 0xbfb8aa3b, v7
	v_mul_f32_e32 v6, 0xbfb8aa3b, v160
	v_mul_f32_e32 v7, 0xbfb8aa3b, v161
	v_exp_f32_e32 v6, v6
	v_exp_f32_e32 v7, v7
	v_lshlrev_b32_e32 v4, 16, v0
	v_and_b32_e32 v5, 0xffff0000, v0
	v_mul_f32_e32 v0, 0xbfb8aa3b, v4
	v_pk_add_f32 v[6:7], v[6:7], 1.0 op_sel_hi:[1,0]
	v_mul_f32_e32 v4, 0xbfb8aa3b, v8
	v_div_scale_f32 v8, s[2:3], v7, v7, 1.0
	v_mul_f32_e32 v1, 0xbfb8aa3b, v5
	v_mul_f32_e32 v5, 0xbfb8aa3b, v155
	v_rcp_f32_e32 v155, v8
	v_exp_f32_e32 v4, v4
	v_exp_f32_e32 v5, v5
	v_exp_f32_e32 v2, v2
	v_fma_f32 v160, -v8, v155, 1.0
	v_fmac_f32_e32 v155, v160, v155
	v_div_scale_f32 v160, vcc, 1.0, v7, 1.0
	v_mul_f32_e32 v161, v160, v155
	v_fma_f32 v164, -v8, v161, v160
	v_fmac_f32_e32 v161, v164, v155
	v_fma_f32 v8, -v8, v161, v160
	v_div_fmas_f32 v8, v8, v155, v161
	v_div_fixup_f32 v7, v8, v7, 1.0
	v_div_scale_f32 v8, s[2:3], v6, v6, 1.0
	v_rcp_f32_e32 v155, v8
	v_pk_add_f32 v[4:5], v[4:5], 1.0 op_sel_hi:[1,0]
	v_exp_f32_e32 v3, v3
	v_exp_f32_e32 v0, v0
	v_fma_f32 v160, -v8, v155, 1.0
	v_fmac_f32_e32 v155, v160, v155
	v_div_scale_f32 v160, vcc, 1.0, v6, 1.0
	v_mul_f32_e32 v161, v160, v155
	v_fma_f32 v164, -v8, v161, v160
	v_fmac_f32_e32 v161, v164, v155
	v_fma_f32 v8, -v8, v161, v160
	v_div_fmas_f32 v8, v8, v155, v161
	v_div_fixup_f32 v6, v8, v6, 1.0
	v_div_scale_f32 v8, s[2:3], v5, v5, 1.0
	v_rcp_f32_e32 v155, v8
	v_pk_add_f32 v[2:3], v[2:3], 1.0 op_sel_hi:[1,0]
	v_exp_f32_e32 v1, v1
	v_fma_f32 v160, -v8, v155, 1.0
	v_fmac_f32_e32 v155, v160, v155
	v_div_scale_f32 v160, vcc, 1.0, v5, 1.0
	v_mul_f32_e32 v161, v160, v155
	v_fma_f32 v164, -v8, v161, v160
	v_fmac_f32_e32 v161, v164, v155
	v_fma_f32 v8, -v8, v161, v160
	v_div_fmas_f32 v8, v8, v155, v161
	v_div_fixup_f32 v5, v8, v5, 1.0
	v_div_scale_f32 v8, s[2:3], v4, v4, 1.0
	v_rcp_f32_e32 v155, v8
	v_pk_add_f32 v[0:1], v[0:1], 1.0 op_sel_hi:[1,0]
	v_fma_f32 v160, -v8, v155, 1.0
	v_fmac_f32_e32 v155, v160, v155
	v_div_scale_f32 v160, vcc, 1.0, v4, 1.0
	v_mul_f32_e32 v161, v160, v155
	v_fma_f32 v164, -v8, v161, v160
	v_fmac_f32_e32 v161, v164, v155
	v_fma_f32 v8, -v8, v161, v160
	v_div_fmas_f32 v8, v8, v155, v161
	v_div_fixup_f32 v4, v8, v4, 1.0
	v_div_scale_f32 v8, s[2:3], v3, v3, 1.0
	v_rcp_f32_e32 v155, v8
	s_nop 0
	v_fma_f32 v160, -v8, v155, 1.0
	v_fmac_f32_e32 v155, v160, v155
	v_div_scale_f32 v160, vcc, 1.0, v3, 1.0
	v_mul_f32_e32 v161, v160, v155
	v_fma_f32 v164, -v8, v161, v160
	v_fmac_f32_e32 v161, v164, v155
	v_fma_f32 v8, -v8, v161, v160
	v_div_fmas_f32 v8, v8, v155, v161
	v_div_fixup_f32 v3, v8, v3, 1.0
	v_div_scale_f32 v8, s[2:3], v2, v2, 1.0
	v_rcp_f32_e32 v155, v8
	s_nop 0
	v_fma_f32 v160, -v8, v155, 1.0
	v_fmac_f32_e32 v155, v160, v155
	v_div_scale_f32 v160, vcc, 1.0, v2, 1.0
	v_mul_f32_e32 v161, v160, v155
	v_fma_f32 v164, -v8, v161, v160
	v_fmac_f32_e32 v161, v164, v155
	v_fma_f32 v8, -v8, v161, v160
	v_div_fmas_f32 v8, v8, v155, v161
	v_div_fixup_f32 v2, v8, v2, 1.0
	v_div_scale_f32 v8, s[2:3], v1, v1, 1.0
	v_rcp_f32_e32 v155, v8
	s_nop 0
	v_fma_f32 v160, -v8, v155, 1.0
	v_fmac_f32_e32 v155, v160, v155
	v_div_scale_f32 v160, vcc, 1.0, v1, 1.0
	v_mul_f32_e32 v161, v160, v155
	v_fma_f32 v164, -v8, v161, v160
	v_fmac_f32_e32 v161, v164, v155
	v_fma_f32 v8, -v8, v161, v160
	v_div_fmas_f32 v8, v8, v155, v161
	v_div_fixup_f32 v1, v8, v1, 1.0
	v_div_scale_f32 v8, s[2:3], v0, v0, 1.0
	v_rcp_f32_e32 v155, v8
	s_mov_b64 s[2:3], 0
	v_fma_f32 v160, -v8, v155, 1.0
	v_fmac_f32_e32 v155, v160, v155
	v_div_scale_f32 v160, vcc, 1.0, v0, 1.0
	v_mul_f32_e32 v161, v160, v155
	v_fma_f32 v164, -v8, v161, v160
	v_fmac_f32_e32 v161, v164, v155
	v_fma_f32 v8, -v8, v161, v160
	v_div_fmas_f32 v8, v8, v155, v161
	v_div_fixup_f32 v0, v8, v0, 1.0

; __device__ __forceinline__ float sigmoidf_(float x) { return 1.0f / (1.0f + __expf(-x)); }
;     __device__ __forceinline__ void operator()(AccMut acc, const Unit& u, int wr, int wc, int, int) const {
;     ...
;                     const int row = row0 + ai * 128 + m * 16, col = col0 + bj * 128;
;                     const bf16* gp = PROJ + (size_t)row * DINP + GATE_OFF + col;
;                     float sc[8];
;                     if (u.seg < 2) {
;                         const v4u ga = *(const v4u*)(gp + u.seg * D), gb = *(const v4u*)(gp + (u.seg + 1) * D);
;                         const float la[8] = {bflo(ga.x), bfhi(ga.x), bflo(ga.y), bfhi(ga.y), bflo(ga.z), bfhi(ga.z), bflo(ga.w), bfhi(ga.w)};
;                         const float lb[8] = {bflo(gb.x), bfhi(gb.x), bflo(gb.y), bfhi(gb.y), bflo(gb.z), bfhi(gb.z), bflo(gb.w), bfhi(gb.w)};
; #pragma unroll
;                         for (int j = 0; j < 8; ++j) { const float ea = __expf(-fminf(fmaxf(la[j], -30.f), 30.f)), eb = __expf(-fminf(fmaxf(lb[j], -30.f), 30.f)); sc[j] = (1.0f + eb) * __builtin_amdgcn_rcpf(1.0f + ea); }
;                     } else {
;                         const v4u ga = *(const v4u*)(gp + 2 * D);
;                         const float la[8] = {bflo(ga.x), bfhi(ga.x), bflo(ga.y), bfhi(ga.y), bflo(ga.z), bfhi(ga.z), bflo(ga.w), bfhi(ga.w)};
; #pragma unroll
;                         for (int j = 0; j < 8; ++j) sc[j] = sigmoidf_(la[j]);
.LBB0_941:
	v_or_b32_e32 v158, 32, v154
	v_mov_b64_e32 v[0:1], s[8:9]
	v_mad_i64_i32 v[0:1], s[2:3], v158, s91, v[0:1]
	s_andn2_b64 vcc, exec, s[22:23]
	v_lshl_add_u64 v[156:157], v[0:1], 0, s[56:57]
	v_lshl_add_u64 v[160:161], v[150:151], 1, v[156:157]
	s_and_b64 vcc, exec, s[6:7]
	s_mov_b64 s[2:3], -1
	s_cbranch_vccnz .LBB0_943
	v_add_co_u32_e32 v0, vcc, 0x2000, v160
	s_nop 1
	v_addc_co_u32_e32 v1, vcc, 0, v161, vcc
	global_load_dwordx4 v[0:3], v[0:1], off nt
	s_waitcnt vmcnt(0)
	v_lshlrev_b32_e32 v6, 16, v1
	v_and_b32_e32 v7, 0xffff0000, v1
	v_lshlrev_b32_e32 v159, 16, v3
	v_and_b32_e32 v164, 0xffff0000, v3
	v_lshlrev_b32_e32 v8, 16, v2
	v_and_b32_e32 v155, 0xffff0000, v2
	v_mul_f32_e32 v2, 0xbfb8aa3b, v6
	v_mul_f32_e32 v3, 0xbfb8aa3b, v7
	v_mul_f32_e32 v6, 0xbfb8aa3b, v159
	v_mul_f32_e32 v7, 0xbfb8aa3b, v164
	v_exp_f32_e32 v6, v6
	v_exp_f32_e32 v7, v7
	v_lshlrev_b32_e32 v4, 16, v0
	v_and_b32_e32 v5, 0xffff0000, v0
	v_mul_f32_e32 v0, 0xbfb8aa3b, v4
	v_pk_add_f32 v[6:7], v[6:7], 1.0 op_sel_hi:[1,0]
	v_mul_f32_e32 v4, 0xbfb8aa3b, v8
	v_div_scale_f32 v8, s[2:3], v7, v7, 1.0
	v_mul_f32_e32 v1, 0xbfb8aa3b, v5
	v_mul_f32_e32 v5, 0xbfb8aa3b, v155
	v_rcp_f32_e32 v155, v8
	v_exp_f32_e32 v4, v4
	v_exp_f32_e32 v5, v5
	v_exp_f32_e32 v2, v2
	v_fma_f32 v159, -v8, v155, 1.0
	v_fmac_f32_e32 v155, v159, v155
	v_div_scale_f32 v159, vcc, 1.0, v7, 1.0
	v_mul_f32_e32 v164, v159, v155
	v_fma_f32 v165, -v8, v164, v159
	v_fmac_f32_e32 v164, v165, v155
	v_fma_f32 v8, -v8, v164, v159
	v_div_fmas_f32 v8, v8, v155, v164
	v_div_fixup_f32 v7, v8, v7, 1.0
	v_div_scale_f32 v8, s[2:3], v6, v6, 1.0
	v_rcp_f32_e32 v155, v8
	v_pk_add_f32 v[4:5], v[4:5], 1.0 op_sel_hi:[1,0]
	v_exp_f32_e32 v3, v3
	v_exp_f32_e32 v0, v0
	v_fma_f32 v159, -v8, v155, 1.0
	v_fmac_f32_e32 v155, v159, v155
	v_div_scale_f32 v159, vcc, 1.0, v6, 1.0
	v_mul_f32_e32 v164, v159, v155
	v_fma_f32 v165, -v8, v164, v159
	v_fmac_f32_e32 v164, v165, v155
	v_fma_f32 v8, -v8, v164, v159
	v_div_fmas_f32 v8, v8, v155, v164
	v_div_fixup_f32 v6, v8, v6, 1.0
	v_div_scale_f32 v8, s[2:3], v5, v5, 1.0
	v_rcp_f32_e32 v155, v8
	v_pk_add_f32 v[2:3], v[2:3], 1.0 op_sel_hi:[1,0]
	v_exp_f32_e32 v1, v1
	v_fma_f32 v159, -v8, v155, 1.0
	v_fmac_f32_e32 v155, v159, v155
	v_div_scale_f32 v159, vcc, 1.0, v5, 1.0
	v_mul_f32_e32 v164, v159, v155
	v_fma_f32 v165, -v8, v164, v159
	v_fmac_f32_e32 v164, v165, v155
	v_fma_f32 v8, -v8, v164, v159
	v_div_fmas_f32 v8, v8, v155, v164
	v_div_fixup_f32 v5, v8, v5, 1.0
	v_div_scale_f32 v8, s[2:3], v4, v4, 1.0
	v_rcp_f32_e32 v155, v8
	v_pk_add_f32 v[0:1], v[0:1], 1.0 op_sel_hi:[1,0]
	v_fma_f32 v159, -v8, v155, 1.0
	v_fmac_f32_e32 v155, v159, v155
	v_div_scale_f32 v159, vcc, 1.0, v4, 1.0
	v_mul_f32_e32 v164, v159, v155
	v_fma_f32 v165, -v8, v164, v159
	v_fmac_f32_e32 v164, v165, v155
	v_fma_f32 v8, -v8, v164, v159
	v_div_fmas_f32 v8, v8, v155, v164
	v_div_fixup_f32 v4, v8, v4, 1.0
	v_div_scale_f32 v8, s[2:3], v3, v3, 1.0
	v_rcp_f32_e32 v155, v8
	s_nop 0
	v_fma_f32 v159, -v8, v155, 1.0
	v_fmac_f32_e32 v155, v159, v155
	v_div_scale_f32 v159, vcc, 1.0, v3, 1.0
	v_mul_f32_e32 v164, v159, v155
	v_fma_f32 v165, -v8, v164, v159
	v_fmac_f32_e32 v164, v165, v155
	v_fma_f32 v8, -v8, v164, v159
	v_div_fmas_f32 v8, v8, v155, v164
	v_div_fixup_f32 v3, v8, v3, 1.0
	v_div_scale_f32 v8, s[2:3], v2, v2, 1.0
	v_rcp_f32_e32 v155, v8
	s_nop 0
	v_fma_f32 v159, -v8, v155, 1.0
	v_fmac_f32_e32 v155, v159, v155
	v_div_scale_f32 v159, vcc, 1.0, v2, 1.0
	v_mul_f32_e32 v164, v159, v155
	v_fma_f32 v165, -v8, v164, v159
	v_fmac_f32_e32 v164, v165, v155
	v_fma_f32 v8, -v8, v164, v159
	v_div_fmas_f32 v8, v8, v155, v164
	v_div_fixup_f32 v2, v8, v2, 1.0
	v_div_scale_f32 v8, s[2:3], v1, v1, 1.0
	v_rcp_f32_e32 v155, v8
	s_nop 0
	v_fma_f32 v159, -v8, v155, 1.0
	v_fmac_f32_e32 v155, v159, v155
	v_div_scale_f32 v159, vcc, 1.0, v1, 1.0
	v_mul_f32_e32 v164, v159, v155
	v_fma_f32 v165, -v8, v164, v159
	v_fmac_f32_e32 v164, v165, v155
	v_fma_f32 v8, -v8, v164, v159
	v_div_fmas_f32 v8, v8, v155, v164
	v_div_fixup_f32 v1, v8, v1, 1.0
	v_div_scale_f32 v8, s[2:3], v0, v0, 1.0
	v_rcp_f32_e32 v155, v8
	s_mov_b64 s[2:3], 0
	v_fma_f32 v159, -v8, v155, 1.0
	v_fmac_f32_e32 v155, v159, v155
	v_div_scale_f32 v159, vcc, 1.0, v0, 1.0
	v_mul_f32_e32 v164, v159, v155
	v_fma_f32 v165, -v8, v164, v159
	v_fmac_f32_e32 v164, v165, v155
	v_fma_f32 v8, -v8, v164, v159
	v_div_fmas_f32 v8, v8, v155, v164
	v_div_fixup_f32 v0, v8, v0, 1.0

; __device__ __forceinline__ float sigmoidf_(float x) { return 1.0f / (1.0f + __expf(-x)); }
;     __device__ __forceinline__ void operator()(AccMut acc, const Unit& u, int wr, int wc, int, int) const {
;     ...
;                     const int row = row0 + ai * 128 + m * 16, col = col0 + bj * 128;
;                     const bf16* gp = PROJ + (size_t)row * DINP + GATE_OFF + col;
;                     float sc[8];
;                     if (u.seg < 2) {
;                         const v4u ga = *(const v4u*)(gp + u.seg * D), gb = *(const v4u*)(gp + (u.seg + 1) * D);
;                         const float la[8] = {bflo(ga.x), bfhi(ga.x), bflo(ga.y), bfhi(ga.y), bflo(ga.z), bfhi(ga.z), bflo(ga.w), bfhi(ga.w)};
;                         const float lb[8] = {bflo(gb.x), bfhi(gb.x), bflo(gb.y), bfhi(gb.y), bflo(gb.z), bfhi(gb.z), bflo(gb.w), bfhi(gb.w)};
; #pragma unroll
;                         for (int j = 0; j < 8; ++j) { const float ea = __expf(-fminf(fmaxf(la[j], -30.f), 30.f)), eb = __expf(-fminf(fmaxf(lb[j], -30.f), 30.f)); sc[j] = (1.0f + eb) * __builtin_amdgcn_rcpf(1.0f + ea); }
;                     } else {
;                         const v4u ga = *(const v4u*)(gp + 2 * D);
;                         const float la[8] = {bflo(ga.x), bfhi(ga.x), bflo(ga.y), bfhi(ga.y), bflo(ga.z), bfhi(ga.z), bflo(ga.w), bfhi(ga.w)};
; #pragma unroll
;                         for (int j = 0; j < 8; ++j) sc[j] = sigmoidf_(la[j]);
.LBB0_954:
	v_or_b32_e32 v158, 48, v154
	v_mov_b64_e32 v[0:1], s[8:9]
	v_mad_i64_i32 v[0:1], s[2:3], v158, s91, v[0:1]
	s_andn2_b64 vcc, exec, s[22:23]
	v_lshl_add_u64 v[156:157], v[0:1], 0, s[56:57]
	v_lshl_add_u64 v[160:161], v[150:151], 1, v[156:157]
	s_and_b64 vcc, exec, s[6:7]
	s_mov_b64 s[2:3], -1
	s_cbranch_vccnz .LBB0_956
	v_add_co_u32_e32 v0, vcc, 0x2000, v160
	s_nop 1
	v_addc_co_u32_e32 v1, vcc, 0, v161, vcc
	global_load_dwordx4 v[0:3], v[0:1], off nt
	s_waitcnt vmcnt(0)
	v_lshlrev_b32_e32 v6, 16, v1
	v_and_b32_e32 v7, 0xffff0000, v1
	v_lshlrev_b32_e32 v159, 16, v3
	v_and_b32_e32 v164, 0xffff0000, v3
	v_lshlrev_b32_e32 v8, 16, v2
	v_and_b32_e32 v155, 0xffff0000, v2
	v_mul_f32_e32 v2, 0xbfb8aa3b, v6
	v_mul_f32_e32 v3, 0xbfb8aa3b, v7
	v_mul_f32_e32 v6, 0xbfb8aa3b, v159
	v_mul_f32_e32 v7, 0xbfb8aa3b, v164
	v_exp_f32_e32 v6, v6
	v_exp_f32_e32 v7, v7
	v_lshlrev_b32_e32 v4, 16, v0
	v_and_b32_e32 v5, 0xffff0000, v0
	v_mul_f32_e32 v0, 0xbfb8aa3b, v4
	v_pk_add_f32 v[6:7], v[6:7], 1.0 op_sel_hi:[1,0]
	v_mul_f32_e32 v4, 0xbfb8aa3b, v8
	v_div_scale_f32 v8, s[2:3], v7, v7, 1.0
	v_mul_f32_e32 v1, 0xbfb8aa3b, v5
	v_mul_f32_e32 v5, 0xbfb8aa3b, v155
	v_rcp_f32_e32 v155, v8
	v_exp_f32_e32 v4, v4
	v_exp_f32_e32 v5, v5
	v_exp_f32_e32 v2, v2
	v_fma_f32 v159, -v8, v155, 1.0
	v_fmac_f32_e32 v155, v159, v155
	v_div_scale_f32 v159, vcc, 1.0, v7, 1.0
	v_mul_f32_e32 v164, v159, v155
	v_fma_f32 v165, -v8, v164, v159
	v_fmac_f32_e32 v164, v165, v155
	v_fma_f32 v8, -v8, v164, v159
	v_div_fmas_f32 v8, v8, v155, v164
	v_div_fixup_f32 v7, v8, v7, 1.0
	v_div_scale_f32 v8, s[2:3], v6, v6, 1.0
	v_rcp_f32_e32 v155, v8
	v_pk_add_f32 v[4:5], v[4:5], 1.0 op_sel_hi:[1,0]
	v_exp_f32_e32 v3, v3
	v_exp_f32_e32 v0, v0
	v_fma_f32 v159, -v8, v155, 1.0
	v_fmac_f32_e32 v155, v159, v155
	v_div_scale_f32 v159, vcc, 1.0, v6, 1.0
	v_mul_f32_e32 v164, v159, v155
	v_fma_f32 v165, -v8, v164, v159
	v_fmac_f32_e32 v164, v165, v155
	v_fma_f32 v8, -v8, v164, v159
	v_div_fmas_f32 v8, v8, v155, v164
	v_div_fixup_f32 v6, v8, v6, 1.0
	v_div_scale_f32 v8, s[2:3], v5, v5, 1.0
	v_rcp_f32_e32 v155, v8
	v_pk_add_f32 v[2:3], v[2:3], 1.0 op_sel_hi:[1,0]
	v_exp_f32_e32 v1, v1
	v_fma_f32 v159, -v8, v155, 1.0
	v_fmac_f32_e32 v155, v159, v155
	v_div_scale_f32 v159, vcc, 1.0, v5, 1.0
	v_mul_f32_e32 v164, v159, v155
	v_fma_f32 v165, -v8, v164, v159
	v_fmac_f32_e32 v164, v165, v155
	v_fma_f32 v8, -v8, v164, v159
	v_div_fmas_f32 v8, v8, v155, v164
	v_div_fixup_f32 v5, v8, v5, 1.0
	v_div_scale_f32 v8, s[2:3], v4, v4, 1.0
	v_rcp_f32_e32 v155, v8
	v_pk_add_f32 v[0:1], v[0:1], 1.0 op_sel_hi:[1,0]
	v_fma_f32 v159, -v8, v155, 1.0
	v_fmac_f32_e32 v155, v159, v155
	v_div_scale_f32 v159, vcc, 1.0, v4, 1.0
	v_mul_f32_e32 v164, v159, v155
	v_fma_f32 v165, -v8, v164, v159
	v_fmac_f32_e32 v164, v165, v155
	v_fma_f32 v8, -v8, v164, v159
	v_div_fmas_f32 v8, v8, v155, v164
	v_div_fixup_f32 v4, v8, v4, 1.0
	v_div_scale_f32 v8, s[2:3], v3, v3, 1.0
	v_rcp_f32_e32 v155, v8
	s_nop 0
	v_fma_f32 v159, -v8, v155, 1.0
	v_fmac_f32_e32 v155, v159, v155
	v_div_scale_f32 v159, vcc, 1.0, v3, 1.0
	v_mul_f32_e32 v164, v159, v155
	v_fma_f32 v165, -v8, v164, v159
	v_fmac_f32_e32 v164, v165, v155
	v_fma_f32 v8, -v8, v164, v159
	v_div_fmas_f32 v8, v8, v155, v164
	v_div_fixup_f32 v3, v8, v3, 1.0
	v_div_scale_f32 v8, s[2:3], v2, v2, 1.0
	v_rcp_f32_e32 v155, v8
	s_nop 0
	v_fma_f32 v159, -v8, v155, 1.0
	v_fmac_f32_e32 v155, v159, v155
	v_div_scale_f32 v159, vcc, 1.0, v2, 1.0
	v_mul_f32_e32 v164, v159, v155
	v_fma_f32 v165, -v8, v164, v159
	v_fmac_f32_e32 v164, v165, v155
	v_fma_f32 v8, -v8, v164, v159
	v_div_fmas_f32 v8, v8, v155, v164
	v_div_fixup_f32 v2, v8, v2, 1.0
	v_div_scale_f32 v8, s[2:3], v1, v1, 1.0
	v_rcp_f32_e32 v155, v8
	s_nop 0
	v_fma_f32 v159, -v8, v155, 1.0
	v_fmac_f32_e32 v155, v159, v155
	v_div_scale_f32 v159, vcc, 1.0, v1, 1.0
	v_mul_f32_e32 v164, v159, v155
	v_fma_f32 v165, -v8, v164, v159
	v_fmac_f32_e32 v164, v165, v155
	v_fma_f32 v8, -v8, v164, v159
	v_div_fmas_f32 v8, v8, v155, v164
	v_div_fixup_f32 v1, v8, v1, 1.0
	v_div_scale_f32 v8, s[2:3], v0, v0, 1.0
	v_rcp_f32_e32 v155, v8
	s_mov_b64 s[2:3], 0
	v_fma_f32 v159, -v8, v155, 1.0
	v_fmac_f32_e32 v155, v159, v155
	v_div_scale_f32 v159, vcc, 1.0, v0, 1.0
	v_mul_f32_e32 v164, v159, v155
	v_fma_f32 v165, -v8, v164, v159
	v_fmac_f32_e32 v164, v165, v155
	v_fma_f32 v8, -v8, v164, v159
	v_div_fmas_f32 v8, v8, v155, v164
	v_div_fixup_f32 v0, v8, v0, 1.0

; __device__ __forceinline__ float sigmoidf_(float x) { return 1.0f / (1.0f + __expf(-x)); }
;     __device__ __forceinline__ void operator()(AccMut acc, const Unit& u, int wr, int wc, int, int) const {
;     ...
;                     const int row = row0 + ai * 128 + m * 16, col = col0 + bj * 128;
;                     const bf16* gp = PROJ + (size_t)row * DINP + GATE_OFF + col;
;                     float sc[8];
;                     if (u.seg < 2) {
;                         const v4u ga = *(const v4u*)(gp + u.seg * D), gb = *(const v4u*)(gp + (u.seg + 1) * D);
;                         const float la[8] = {bflo(ga.x), bfhi(ga.x), bflo(ga.y), bfhi(ga.y), bflo(ga.z), bfhi(ga.z), bflo(ga.w), bfhi(ga.w)};
;                         const float lb[8] = {bflo(gb.x), bfhi(gb.x), bflo(gb.y), bfhi(gb.y), bflo(gb.z), bfhi(gb.z), bflo(gb.w), bfhi(gb.w)};
; #pragma unroll
;                         for (int j = 0; j < 8; ++j) { const float ea = __expf(-fminf(fmaxf(la[j], -30.f), 30.f)), eb = __expf(-fminf(fmaxf(lb[j], -30.f), 30.f)); sc[j] = (1.0f + eb) * __builtin_amdgcn_rcpf(1.0f + ea); }
;                     } else {
;                         const v4u ga = *(const v4u*)(gp + 2 * D);
;                         const float la[8] = {bflo(ga.x), bfhi(ga.x), bflo(ga.y), bfhi(ga.y), bflo(ga.z), bfhi(ga.z), bflo(ga.w), bfhi(ga.w)};
; #pragma unroll
;                         for (int j = 0; j < 8; ++j) sc[j] = sigmoidf_(la[j]);
.LBB0_967:
	v_add_u32_e32 v158, 0x80, v154
	v_mov_b64_e32 v[0:1], s[8:9]
	v_mad_i64_i32 v[0:1], s[2:3], v158, s91, v[0:1]
	s_andn2_b64 vcc, exec, s[22:23]
	v_lshl_add_u64 v[156:157], v[0:1], 0, s[56:57]
	v_lshl_add_u64 v[160:161], v[150:151], 1, v[156:157]
	s_and_b64 vcc, exec, s[6:7]
	s_mov_b64 s[2:3], -1
	s_cbranch_vccnz .LBB0_969
	v_add_co_u32_e32 v0, vcc, 0x2000, v160
	s_nop 1
	v_addc_co_u32_e32 v1, vcc, 0, v161, vcc
	global_load_dwordx4 v[0:3], v[0:1], off nt
	s_waitcnt vmcnt(0)
	v_lshlrev_b32_e32 v6, 16, v1
	v_and_b32_e32 v7, 0xffff0000, v1
	v_lshlrev_b32_e32 v159, 16, v3
	v_and_b32_e32 v164, 0xffff0000, v3
	v_lshlrev_b32_e32 v8, 16, v2
	v_and_b32_e32 v155, 0xffff0000, v2
	v_mul_f32_e32 v2, 0xbfb8aa3b, v6
	v_mul_f32_e32 v3, 0xbfb8aa3b, v7
	v_mul_f32_e32 v6, 0xbfb8aa3b, v159
	v_mul_f32_e32 v7, 0xbfb8aa3b, v164
	v_exp_f32_e32 v6, v6
	v_exp_f32_e32 v7, v7
	v_lshlrev_b32_e32 v4, 16, v0
	v_and_b32_e32 v5, 0xffff0000, v0
	v_mul_f32_e32 v0, 0xbfb8aa3b, v4
	v_pk_add_f32 v[6:7], v[6:7], 1.0 op_sel_hi:[1,0]
	v_mul_f32_e32 v4, 0xbfb8aa3b, v8
	v_div_scale_f32 v8, s[2:3], v7, v7, 1.0
	v_mul_f32_e32 v1, 0xbfb8aa3b, v5
	v_mul_f32_e32 v5, 0xbfb8aa3b, v155
	v_rcp_f32_e32 v155, v8
	v_exp_f32_e32 v4, v4
	v_exp_f32_e32 v5, v5
	v_exp_f32_e32 v2, v2
	v_fma_f32 v159, -v8, v155, 1.0
	v_fmac_f32_e32 v155, v159, v155
	v_div_scale_f32 v159, vcc, 1.0, v7, 1.0
	v_mul_f32_e32 v164, v159, v155
	v_fma_f32 v165, -v8, v164, v159
	v_fmac_f32_e32 v164, v165, v155
	v_fma_f32 v8, -v8, v164, v159
	v_div_fmas_f32 v8, v8, v155, v164
	v_div_fixup_f32 v7, v8, v7, 1.0
	v_div_scale_f32 v8, s[2:3], v6, v6, 1.0
	v_rcp_f32_e32 v155, v8
	v_pk_add_f32 v[4:5], v[4:5], 1.0 op_sel_hi:[1,0]
	v_exp_f32_e32 v3, v3
	v_exp_f32_e32 v0, v0
	v_fma_f32 v159, -v8, v155, 1.0
	v_fmac_f32_e32 v155, v159, v155
	v_div_scale_f32 v159, vcc, 1.0, v6, 1.0
	v_mul_f32_e32 v164, v159, v155
	v_fma_f32 v165, -v8, v164, v159
	v_fmac_f32_e32 v164, v165, v155
	v_fma_f32 v8, -v8, v164, v159
	v_div_fmas_f32 v8, v8, v155, v164
	v_div_fixup_f32 v6, v8, v6, 1.0
	v_div_scale_f32 v8, s[2:3], v5, v5, 1.0
	v_rcp_f32_e32 v155, v8
	v_pk_add_f32 v[2:3], v[2:3], 1.0 op_sel_hi:[1,0]
	v_exp_f32_e32 v1, v1
	v_fma_f32 v159, -v8, v155, 1.0
	v_fmac_f32_e32 v155, v159, v155
	v_div_scale_f32 v159, vcc, 1.0, v5, 1.0
	v_mul_f32_e32 v164, v159, v155
	v_fma_f32 v165, -v8, v164, v159
	v_fmac_f32_e32 v164, v165, v155
	v_fma_f32 v8, -v8, v164, v159
	v_div_fmas_f32 v8, v8, v155, v164
	v_div_fixup_f32 v5, v8, v5, 1.0
	v_div_scale_f32 v8, s[2:3], v4, v4, 1.0
	v_rcp_f32_e32 v155, v8
	v_pk_add_f32 v[0:1], v[0:1], 1.0 op_sel_hi:[1,0]
	v_fma_f32 v159, -v8, v155, 1.0
	v_fmac_f32_e32 v155, v159, v155
	v_div_scale_f32 v159, vcc, 1.0, v4, 1.0
	v_mul_f32_e32 v164, v159, v155
	v_fma_f32 v165, -v8, v164, v159
	v_fmac_f32_e32 v164, v165, v155
	v_fma_f32 v8, -v8, v164, v159
	v_div_fmas_f32 v8, v8, v155, v164
	v_div_fixup_f32 v4, v8, v4, 1.0
	v_div_scale_f32 v8, s[2:3], v3, v3, 1.0
	v_rcp_f32_e32 v155, v8
	s_nop 0
	v_fma_f32 v159, -v8, v155, 1.0
	v_fmac_f32_e32 v155, v159, v155
	v_div_scale_f32 v159, vcc, 1.0, v3, 1.0
	v_mul_f32_e32 v164, v159, v155
	v_fma_f32 v165, -v8, v164, v159
	v_fmac_f32_e32 v164, v165, v155
	v_fma_f32 v8, -v8, v164, v159
	v_div_fmas_f32 v8, v8, v155, v164
	v_div_fixup_f32 v3, v8, v3, 1.0
	v_div_scale_f32 v8, s[2:3], v2, v2, 1.0
	v_rcp_f32_e32 v155, v8
	s_nop 0
	v_fma_f32 v159, -v8, v155, 1.0
	v_fmac_f32_e32 v155, v159, v155
	v_div_scale_f32 v159, vcc, 1.0, v2, 1.0
	v_mul_f32_e32 v164, v159, v155
	v_fma_f32 v165, -v8, v164, v159
	v_fmac_f32_e32 v164, v165, v155
	v_fma_f32 v8, -v8, v164, v159
	v_div_fmas_f32 v8, v8, v155, v164
	v_div_fixup_f32 v2, v8, v2, 1.0
	v_div_scale_f32 v8, s[2:3], v1, v1, 1.0
	v_rcp_f32_e32 v155, v8
	s_nop 0
	v_fma_f32 v159, -v8, v155, 1.0
	v_fmac_f32_e32 v155, v159, v155
	v_div_scale_f32 v159, vcc, 1.0, v1, 1.0
	v_mul_f32_e32 v164, v159, v155
	v_fma_f32 v165, -v8, v164, v159
	v_fmac_f32_e32 v164, v165, v155
	v_fma_f32 v8, -v8, v164, v159
	v_div_fmas_f32 v8, v8, v155, v164
	v_div_fixup_f32 v1, v8, v1, 1.0
	v_div_scale_f32 v8, s[2:3], v0, v0, 1.0
	v_rcp_f32_e32 v155, v8
	s_mov_b64 s[2:3], 0
	v_fma_f32 v159, -v8, v155, 1.0
	v_fmac_f32_e32 v155, v159, v155
	v_div_scale_f32 v159, vcc, 1.0, v0, 1.0
	v_mul_f32_e32 v164, v159, v155
	v_fma_f32 v165, -v8, v164, v159
	v_fmac_f32_e32 v164, v165, v155
	v_fma_f32 v8, -v8, v164, v159
	v_div_fmas_f32 v8, v8, v155, v164
	v_div_fixup_f32 v0, v8, v0, 1.0

; __device__ __forceinline__ float sigmoidf_(float x) { return 1.0f / (1.0f + __expf(-x)); }
;     __device__ __forceinline__ void operator()(AccMut acc, const Unit& u, int wr, int wc, int, int) const {
;     ...
;                     const int row = row0 + ai * 128 + m * 16, col = col0 + bj * 128;
;                     const bf16* gp = PROJ + (size_t)row * DINP + GATE_OFF + col;
;                     float sc[8];
;                     if (u.seg < 2) {
;                         const v4u ga = *(const v4u*)(gp + u.seg * D), gb = *(const v4u*)(gp + (u.seg + 1) * D);
;                         const float la[8] = {bflo(ga.x), bfhi(ga.x), bflo(ga.y), bfhi(ga.y), bflo(ga.z), bfhi(ga.z), bflo(ga.w), bfhi(ga.w)};
;                         const float lb[8] = {bflo(gb.x), bfhi(gb.x), bflo(gb.y), bfhi(gb.y), bflo(gb.z), bfhi(gb.z), bflo(gb.w), bfhi(gb.w)};
; #pragma unroll
;                         for (int j = 0; j < 8; ++j) { const float ea = __expf(-fminf(fmaxf(la[j], -30.f), 30.f)), eb = __expf(-fminf(fmaxf(lb[j], -30.f), 30.f)); sc[j] = (1.0f + eb) * __builtin_amdgcn_rcpf(1.0f + ea); }
;                     } else {
;                         const v4u ga = *(const v4u*)(gp + 2 * D);
;                         const float la[8] = {bflo(ga.x), bfhi(ga.x), bflo(ga.y), bfhi(ga.y), bflo(ga.z), bfhi(ga.z), bflo(ga.w), bfhi(ga.w)};
; #pragma unroll
;                         for (int j = 0; j < 8; ++j) sc[j] = sigmoidf_(la[j]);
.LBB0_980:
	v_add_u32_e32 v158, 0x90, v154
	v_mov_b64_e32 v[0:1], s[8:9]
	v_mad_i64_i32 v[0:1], s[2:3], v158, s91, v[0:1]
	s_andn2_b64 vcc, exec, s[22:23]
	v_lshl_add_u64 v[156:157], v[0:1], 0, s[56:57]
	v_lshl_add_u64 v[160:161], v[150:151], 1, v[156:157]
	s_and_b64 vcc, exec, s[6:7]
	s_mov_b64 s[2:3], -1
	s_cbranch_vccnz .LBB0_982
	v_add_co_u32_e32 v0, vcc, 0x2000, v160
	s_nop 1
	v_addc_co_u32_e32 v1, vcc, 0, v161, vcc
	global_load_dwordx4 v[0:3], v[0:1], off nt
	s_waitcnt vmcnt(0)
	v_lshlrev_b32_e32 v6, 16, v1
	v_and_b32_e32 v7, 0xffff0000, v1
	v_lshlrev_b32_e32 v159, 16, v3
	v_and_b32_e32 v164, 0xffff0000, v3
	v_lshlrev_b32_e32 v8, 16, v2
	v_and_b32_e32 v155, 0xffff0000, v2
	v_mul_f32_e32 v2, 0xbfb8aa3b, v6
	v_mul_f32_e32 v3, 0xbfb8aa3b, v7
	v_mul_f32_e32 v6, 0xbfb8aa3b, v159
	v_mul_f32_e32 v7, 0xbfb8aa3b, v164
	v_exp_f32_e32 v6, v6
	v_exp_f32_e32 v7, v7
	v_lshlrev_b32_e32 v4, 16, v0
	v_and_b32_e32 v5, 0xffff0000, v0
	v_mul_f32_e32 v0, 0xbfb8aa3b, v4
	v_pk_add_f32 v[6:7], v[6:7], 1.0 op_sel_hi:[1,0]
	v_mul_f32_e32 v4, 0xbfb8aa3b, v8
	v_div_scale_f32 v8, s[2:3], v7, v7, 1.0
	v_mul_f32_e32 v1, 0xbfb8aa3b, v5
	v_mul_f32_e32 v5, 0xbfb8aa3b, v155
	v_rcp_f32_e32 v155, v8
	v_exp_f32_e32 v4, v4
	v_exp_f32_e32 v5, v5
	v_exp_f32_e32 v2, v2
	v_fma_f32 v159, -v8, v155, 1.0
	v_fmac_f32_e32 v155, v159, v155
	v_div_scale_f32 v159, vcc, 1.0, v7, 1.0
	v_mul_f32_e32 v164, v159, v155
	v_fma_f32 v165, -v8, v164, v159
	v_fmac_f32_e32 v164, v165, v155
	v_fma_f32 v8, -v8, v164, v159
	v_div_fmas_f32 v8, v8, v155, v164
	v_div_fixup_f32 v7, v8, v7, 1.0
	v_div_scale_f32 v8, s[2:3], v6, v6, 1.0
	v_rcp_f32_e32 v155, v8
	v_pk_add_f32 v[4:5], v[4:5], 1.0 op_sel_hi:[1,0]
	v_exp_f32_e32 v3, v3
	v_exp_f32_e32 v0, v0
	v_fma_f32 v159, -v8, v155, 1.0
	v_fmac_f32_e32 v155, v159, v155
	v_div_scale_f32 v159, vcc, 1.0, v6, 1.0
	v_mul_f32_e32 v164, v159, v155
	v_fma_f32 v165, -v8, v164, v159
	v_fmac_f32_e32 v164, v165, v155
	v_fma_f32 v8, -v8, v164, v159
	v_div_fmas_f32 v8, v8, v155, v164
	v_div_fixup_f32 v6, v8, v6, 1.0
	v_div_scale_f32 v8, s[2:3], v5, v5, 1.0
	v_rcp_f32_e32 v155, v8
	v_pk_add_f32 v[2:3], v[2:3], 1.0 op_sel_hi:[1,0]
	v_exp_f32_e32 v1, v1
	v_fma_f32 v159, -v8, v155, 1.0
	v_fmac_f32_e32 v155, v159, v155
	v_div_scale_f32 v159, vcc, 1.0, v5, 1.0
	v_mul_f32_e32 v164, v159, v155
	v_fma_f32 v165, -v8, v164, v159
	v_fmac_f32_e32 v164, v165, v155
	v_fma_f32 v8, -v8, v164, v159
	v_div_fmas_f32 v8, v8, v155, v164
	v_div_fixup_f32 v5, v8, v5, 1.0
	v_div_scale_f32 v8, s[2:3], v4, v4, 1.0
	v_rcp_f32_e32 v155, v8
	v_pk_add_f32 v[0:1], v[0:1], 1.0 op_sel_hi:[1,0]
	v_fma_f32 v159, -v8, v155, 1.0
	v_fmac_f32_e32 v155, v159, v155
	v_div_scale_f32 v159, vcc, 1.0, v4, 1.0
	v_mul_f32_e32 v164, v159, v155
	v_fma_f32 v165, -v8, v164, v159
	v_fmac_f32_e32 v164, v165, v155
	v_fma_f32 v8, -v8, v164, v159
	v_div_fmas_f32 v8, v8, v155, v164
	v_div_fixup_f32 v4, v8, v4, 1.0
	v_div_scale_f32 v8, s[2:3], v3, v3, 1.0
	v_rcp_f32_e32 v155, v8
	s_nop 0
	v_fma_f32 v159, -v8, v155, 1.0
	v_fmac_f32_e32 v155, v159, v155
	v_div_scale_f32 v159, vcc, 1.0, v3, 1.0
	v_mul_f32_e32 v164, v159, v155
	v_fma_f32 v165, -v8, v164, v159
	v_fmac_f32_e32 v164, v165, v155
	v_fma_f32 v8, -v8, v164, v159
	v_div_fmas_f32 v8, v8, v155, v164
	v_div_fixup_f32 v3, v8, v3, 1.0
	v_div_scale_f32 v8, s[2:3], v2, v2, 1.0
	v_rcp_f32_e32 v155, v8
	s_nop 0
	v_fma_f32 v159, -v8, v155, 1.0
	v_fmac_f32_e32 v155, v159, v155
	v_div_scale_f32 v159, vcc, 1.0, v2, 1.0
	v_mul_f32_e32 v164, v159, v155
	v_fma_f32 v165, -v8, v164, v159
	v_fmac_f32_e32 v164, v165, v155
	v_fma_f32 v8, -v8, v164, v159
	v_div_fmas_f32 v8, v8, v155, v164
	v_div_fixup_f32 v2, v8, v2, 1.0
	v_div_scale_f32 v8, s[2:3], v1, v1, 1.0
	v_rcp_f32_e32 v155, v8
	s_nop 0
	v_fma_f32 v159, -v8, v155, 1.0
	v_fmac_f32_e32 v155, v159, v155
	v_div_scale_f32 v159, vcc, 1.0, v1, 1.0
	v_mul_f32_e32 v164, v159, v155
	v_fma_f32 v165, -v8, v164, v159
	v_fmac_f32_e32 v164, v165, v155
	v_fma_f32 v8, -v8, v164, v159
	v_div_fmas_f32 v8, v8, v155, v164
	v_div_fixup_f32 v1, v8, v1, 1.0
	v_div_scale_f32 v8, s[2:3], v0, v0, 1.0
	v_rcp_f32_e32 v155, v8
	s_mov_b64 s[2:3], 0
	v_fma_f32 v159, -v8, v155, 1.0
	v_fmac_f32_e32 v155, v159, v155
	v_div_scale_f32 v159, vcc, 1.0, v0, 1.0
	v_mul_f32_e32 v164, v159, v155
	v_fma_f32 v165, -v8, v164, v159
	v_fmac_f32_e32 v164, v165, v155
	v_fma_f32 v8, -v8, v164, v159
	v_div_fmas_f32 v8, v8, v155, v164
	v_div_fixup_f32 v0, v8, v0, 1.0

; __device__ __forceinline__ float sigmoidf_(float x) { return 1.0f / (1.0f + __expf(-x)); }
;     __device__ __forceinline__ void operator()(AccMut acc, const Unit& u, int wr, int wc, int, int) const {
;     ...
;                     const int row = row0 + ai * 128 + m * 16, col = col0 + bj * 128;
;                     const bf16* gp = PROJ + (size_t)row * DINP + GATE_OFF + col;
;                     float sc[8];
;                     if (u.seg < 2) {
;                         const v4u ga = *(const v4u*)(gp + u.seg * D), gb = *(const v4u*)(gp + (u.seg + 1) * D);
;                         const float la[8] = {bflo(ga.x), bfhi(ga.x), bflo(ga.y), bfhi(ga.y), bflo(ga.z), bfhi(ga.z), bflo(ga.w), bfhi(ga.w)};
;                         const float lb[8] = {bflo(gb.x), bfhi(gb.x), bflo(gb.y), bfhi(gb.y), bflo(gb.z), bfhi(gb.z), bflo(gb.w), bfhi(gb.w)};
; #pragma unroll
;                         for (int j = 0; j < 8; ++j) { const float ea = __expf(-fminf(fmaxf(la[j], -30.f), 30.f)), eb = __expf(-fminf(fmaxf(lb[j], -30.f), 30.f)); sc[j] = (1.0f + eb) * __builtin_amdgcn_rcpf(1.0f + ea); }
;                     } else {
;                         const v4u ga = *(const v4u*)(gp + 2 * D);
;                         const float la[8] = {bflo(ga.x), bfhi(ga.x), bflo(ga.y), bfhi(ga.y), bflo(ga.z), bfhi(ga.z), bflo(ga.w), bfhi(ga.w)};
; #pragma unroll
;                         for (int j = 0; j < 8; ++j) sc[j] = sigmoidf_(la[j]);
.LBB0_993:
	v_add_u32_e32 v158, 0xa0, v154
	v_mov_b64_e32 v[0:1], s[8:9]
	v_mad_i64_i32 v[0:1], s[2:3], v158, s91, v[0:1]
	s_andn2_b64 vcc, exec, s[22:23]
	v_lshl_add_u64 v[156:157], v[0:1], 0, s[56:57]
	v_lshl_add_u64 v[160:161], v[150:151], 1, v[156:157]
	s_and_b64 vcc, exec, s[6:7]
	s_mov_b64 s[2:3], -1
	s_cbranch_vccnz .LBB0_995
	v_add_co_u32_e32 v0, vcc, 0x2000, v160
	s_nop 1
	v_addc_co_u32_e32 v1, vcc, 0, v161, vcc
	global_load_dwordx4 v[0:3], v[0:1], off nt
	s_waitcnt vmcnt(0)
	v_lshlrev_b32_e32 v6, 16, v1
	v_and_b32_e32 v7, 0xffff0000, v1
	v_lshlrev_b32_e32 v159, 16, v3
	v_and_b32_e32 v164, 0xffff0000, v3
	v_lshlrev_b32_e32 v8, 16, v2
	v_and_b32_e32 v155, 0xffff0000, v2
	v_mul_f32_e32 v2, 0xbfb8aa3b, v6
	v_mul_f32_e32 v3, 0xbfb8aa3b, v7
	v_mul_f32_e32 v6, 0xbfb8aa3b, v159
	v_mul_f32_e32 v7, 0xbfb8aa3b, v164
	v_exp_f32_e32 v6, v6
	v_exp_f32_e32 v7, v7
	v_lshlrev_b32_e32 v4, 16, v0
	v_and_b32_e32 v5, 0xffff0000, v0
	v_mul_f32_e32 v0, 0xbfb8aa3b, v4
	v_pk_add_f32 v[6:7], v[6:7], 1.0 op_sel_hi:[1,0]
	v_mul_f32_e32 v4, 0xbfb8aa3b, v8
	v_div_scale_f32 v8, s[2:3], v7, v7, 1.0
	v_mul_f32_e32 v1, 0xbfb8aa3b, v5
	v_mul_f32_e32 v5, 0xbfb8aa3b, v155
	v_rcp_f32_e32 v155, v8
	v_exp_f32_e32 v4, v4
	v_exp_f32_e32 v5, v5
	v_exp_f32_e32 v2, v2
	v_fma_f32 v159, -v8, v155, 1.0
	v_fmac_f32_e32 v155, v159, v155
	v_div_scale_f32 v159, vcc, 1.0, v7, 1.0
	v_mul_f32_e32 v164, v159, v155
	v_fma_f32 v165, -v8, v164, v159
	v_fmac_f32_e32 v164, v165, v155
	v_fma_f32 v8, -v8, v164, v159
	v_div_fmas_f32 v8, v8, v155, v164
	v_div_fixup_f32 v7, v8, v7, 1.0
	v_div_scale_f32 v8, s[2:3], v6, v6, 1.0
	v_rcp_f32_e32 v155, v8
	v_pk_add_f32 v[4:5], v[4:5], 1.0 op_sel_hi:[1,0]
	v_exp_f32_e32 v3, v3
	v_exp_f32_e32 v0, v0
	v_fma_f32 v159, -v8, v155, 1.0
	v_fmac_f32_e32 v155, v159, v155
	v_div_scale_f32 v159, vcc, 1.0, v6, 1.0
	v_mul_f32_e32 v164, v159, v155
	v_fma_f32 v165, -v8, v164, v159
	v_fmac_f32_e32 v164, v165, v155
	v_fma_f32 v8, -v8, v164, v159
	v_div_fmas_f32 v8, v8, v155, v164
	v_div_fixup_f32 v6, v8, v6, 1.0
	v_div_scale_f32 v8, s[2:3], v5, v5, 1.0
	v_rcp_f32_e32 v155, v8
	v_pk_add_f32 v[2:3], v[2:3], 1.0 op_sel_hi:[1,0]
	v_exp_f32_e32 v1, v1
	v_fma_f32 v159, -v8, v155, 1.0
	v_fmac_f32_e32 v155, v159, v155
	v_div_scale_f32 v159, vcc, 1.0, v5, 1.0
	v_mul_f32_e32 v164, v159, v155
	v_fma_f32 v165, -v8, v164, v159
	v_fmac_f32_e32 v164, v165, v155
	v_fma_f32 v8, -v8, v164, v159
	v_div_fmas_f32 v8, v8, v155, v164
	v_div_fixup_f32 v5, v8, v5, 1.0
	v_div_scale_f32 v8, s[2:3], v4, v4, 1.0
	v_rcp_f32_e32 v155, v8
	v_pk_add_f32 v[0:1], v[0:1], 1.0 op_sel_hi:[1,0]
	v_fma_f32 v159, -v8, v155, 1.0
	v_fmac_f32_e32 v155, v159, v155
	v_div_scale_f32 v159, vcc, 1.0, v4, 1.0
	v_mul_f32_e32 v164, v159, v155
	v_fma_f32 v165, -v8, v164, v159
	v_fmac_f32_e32 v164, v165, v155
	v_fma_f32 v8, -v8, v164, v159
	v_div_fmas_f32 v8, v8, v155, v164
	v_div_fixup_f32 v4, v8, v4, 1.0
	v_div_scale_f32 v8, s[2:3], v3, v3, 1.0
	v_rcp_f32_e32 v155, v8
	s_nop 0
	v_fma_f32 v159, -v8, v155, 1.0
	v_fmac_f32_e32 v155, v159, v155
	v_div_scale_f32 v159, vcc, 1.0, v3, 1.0
	v_mul_f32_e32 v164, v159, v155
	v_fma_f32 v165, -v8, v164, v159
	v_fmac_f32_e32 v164, v165, v155
	v_fma_f32 v8, -v8, v164, v159
	v_div_fmas_f32 v8, v8, v155, v164
	v_div_fixup_f32 v3, v8, v3, 1.0
	v_div_scale_f32 v8, s[2:3], v2, v2, 1.0
	v_rcp_f32_e32 v155, v8
	s_nop 0
	v_fma_f32 v159, -v8, v155, 1.0
	v_fmac_f32_e32 v155, v159, v155
	v_div_scale_f32 v159, vcc, 1.0, v2, 1.0
	v_mul_f32_e32 v164, v159, v155
	v_fma_f32 v165, -v8, v164, v159
	v_fmac_f32_e32 v164, v165, v155
	v_fma_f32 v8, -v8, v164, v159
	v_div_fmas_f32 v8, v8, v155, v164
	v_div_fixup_f32 v2, v8, v2, 1.0
	v_div_scale_f32 v8, s[2:3], v1, v1, 1.0
	v_rcp_f32_e32 v155, v8
	s_nop 0
	v_fma_f32 v159, -v8, v155, 1.0
	v_fmac_f32_e32 v155, v159, v155
	v_div_scale_f32 v159, vcc, 1.0, v1, 1.0
	v_mul_f32_e32 v164, v159, v155
	v_fma_f32 v165, -v8, v164, v159
	v_fmac_f32_e32 v164, v165, v155
	v_fma_f32 v8, -v8, v164, v159
	v_div_fmas_f32 v8, v8, v155, v164
	v_div_fixup_f32 v1, v8, v1, 1.0
	v_div_scale_f32 v8, s[2:3], v0, v0, 1.0
	v_rcp_f32_e32 v155, v8
	s_mov_b64 s[2:3], 0
	v_fma_f32 v159, -v8, v155, 1.0
	v_fmac_f32_e32 v155, v159, v155
	v_div_scale_f32 v159, vcc, 1.0, v0, 1.0
	v_mul_f32_e32 v164, v159, v155
	v_fma_f32 v165, -v8, v164, v159
	v_fmac_f32_e32 v164, v165, v155
	v_fma_f32 v8, -v8, v164, v159
	v_div_fmas_f32 v8, v8, v155, v164
	v_div_fixup_f32 v0, v8, v0, 1.0

; __device__ __forceinline__ float sigmoidf_(float x) { return 1.0f / (1.0f + __expf(-x)); }
;     __device__ __forceinline__ void operator()(AccMut acc, const Unit& u, int wr, int wc, int, int) const {
;     ...
;                     const int row = row0 + ai * 128 + m * 16, col = col0 + bj * 128;
;                     const bf16* gp = PROJ + (size_t)row * DINP + GATE_OFF + col;
;                     float sc[8];
;                     if (u.seg < 2) {
;                         const v4u ga = *(const v4u*)(gp + u.seg * D), gb = *(const v4u*)(gp + (u.seg + 1) * D);
;                         const float la[8] = {bflo(ga.x), bfhi(ga.x), bflo(ga.y), bfhi(ga.y), bflo(ga.z), bfhi(ga.z), bflo(ga.w), bfhi(ga.w)};
;                         const float lb[8] = {bflo(gb.x), bfhi(gb.x), bflo(gb.y), bfhi(gb.y), bflo(gb.z), bfhi(gb.z), bflo(gb.w), bfhi(gb.w)};
; #pragma unroll
;                         for (int j = 0; j < 8; ++j) { const float ea = __expf(-fminf(fmaxf(la[j], -30.f), 30.f)), eb = __expf(-fminf(fmaxf(lb[j], -30.f), 30.f)); sc[j] = (1.0f + eb) * __builtin_amdgcn_rcpf(1.0f + ea); }
;                     } else {
;                         const v4u ga = *(const v4u*)(gp + 2 * D);
;                         const float la[8] = {bflo(ga.x), bfhi(ga.x), bflo(ga.y), bfhi(ga.y), bflo(ga.z), bfhi(ga.z), bflo(ga.w), bfhi(ga.w)};
; #pragma unroll
;                         for (int j = 0; j < 8; ++j) sc[j] = sigmoidf_(la[j]);
.LBB0_1006:
	v_add_u32_e32 v156, 0xb0, v154
	v_mov_b64_e32 v[0:1], s[8:9]
	v_mad_i64_i32 v[0:1], s[2:3], v156, s91, v[0:1]
	s_andn2_b64 vcc, exec, s[22:23]
	v_lshl_add_u64 v[154:155], v[0:1], 0, s[56:57]
	v_lshl_add_u64 v[158:159], v[150:151], 1, v[154:155]
	s_and_b64 vcc, exec, s[6:7]
	s_mov_b64 s[2:3], -1
	s_cbranch_vccnz .LBB0_1008
	v_add_co_u32_e32 v0, vcc, 0x2000, v158
	s_nop 1
	v_addc_co_u32_e32 v1, vcc, 0, v159, vcc
	global_load_dwordx4 v[0:3], v[0:1], off nt
	s_waitcnt vmcnt(0)
	v_lshlrev_b32_e32 v6, 16, v1
	v_and_b32_e32 v7, 0xffff0000, v1
	v_lshlrev_b32_e32 v160, 16, v3
	v_and_b32_e32 v161, 0xffff0000, v3
	v_lshlrev_b32_e32 v8, 16, v2
	v_and_b32_e32 v157, 0xffff0000, v2
	v_mul_f32_e32 v2, 0xbfb8aa3b, v6
	v_mul_f32_e32 v3, 0xbfb8aa3b, v7
	v_mul_f32_e32 v6, 0xbfb8aa3b, v160
	v_mul_f32_e32 v7, 0xbfb8aa3b, v161
	v_exp_f32_e32 v6, v6
	v_exp_f32_e32 v7, v7
	v_lshlrev_b32_e32 v4, 16, v0
	v_and_b32_e32 v5, 0xffff0000, v0
	v_mul_f32_e32 v0, 0xbfb8aa3b, v4
	v_pk_add_f32 v[6:7], v[6:7], 1.0 op_sel_hi:[1,0]
	v_mul_f32_e32 v4, 0xbfb8aa3b, v8
	v_div_scale_f32 v8, s[2:3], v7, v7, 1.0
	v_mul_f32_e32 v1, 0xbfb8aa3b, v5
	v_mul_f32_e32 v5, 0xbfb8aa3b, v157
	v_rcp_f32_e32 v157, v8
	v_exp_f32_e32 v4, v4
	v_exp_f32_e32 v5, v5
	v_exp_f32_e32 v2, v2
	v_fma_f32 v160, -v8, v157, 1.0
	v_fmac_f32_e32 v157, v160, v157
	v_div_scale_f32 v160, vcc, 1.0, v7, 1.0
	v_mul_f32_e32 v161, v160, v157
	v_fma_f32 v164, -v8, v161, v160
	v_fmac_f32_e32 v161, v164, v157
	v_fma_f32 v8, -v8, v161, v160
	v_div_fmas_f32 v8, v8, v157, v161
	v_div_fixup_f32 v7, v8, v7, 1.0
	v_div_scale_f32 v8, s[2:3], v6, v6, 1.0
	v_rcp_f32_e32 v157, v8
	v_pk_add_f32 v[4:5], v[4:5], 1.0 op_sel_hi:[1,0]
	v_exp_f32_e32 v3, v3
	v_exp_f32_e32 v0, v0
	v_fma_f32 v160, -v8, v157, 1.0
	v_fmac_f32_e32 v157, v160, v157
	v_div_scale_f32 v160, vcc, 1.0, v6, 1.0
	v_mul_f32_e32 v161, v160, v157
	v_fma_f32 v164, -v8, v161, v160
	v_fmac_f32_e32 v161, v164, v157
	v_fma_f32 v8, -v8, v161, v160
	v_div_fmas_f32 v8, v8, v157, v161
	v_div_fixup_f32 v6, v8, v6, 1.0
	v_div_scale_f32 v8, s[2:3], v5, v5, 1.0
	v_rcp_f32_e32 v157, v8
	v_pk_add_f32 v[2:3], v[2:3], 1.0 op_sel_hi:[1,0]
	v_exp_f32_e32 v1, v1
	v_fma_f32 v160, -v8, v157, 1.0
	v_fmac_f32_e32 v157, v160, v157
	v_div_scale_f32 v160, vcc, 1.0, v5, 1.0
	v_mul_f32_e32 v161, v160, v157
	v_fma_f32 v164, -v8, v161, v160
	v_fmac_f32_e32 v161, v164, v157
	v_fma_f32 v8, -v8, v161, v160
	v_div_fmas_f32 v8, v8, v157, v161
	v_div_fixup_f32 v5, v8, v5, 1.0
	v_div_scale_f32 v8, s[2:3], v4, v4, 1.0
	v_rcp_f32_e32 v157, v8
	v_pk_add_f32 v[0:1], v[0:1], 1.0 op_sel_hi:[1,0]
	v_fma_f32 v160, -v8, v157, 1.0
	v_fmac_f32_e32 v157, v160, v157
	v_div_scale_f32 v160, vcc, 1.0, v4, 1.0
	v_mul_f32_e32 v161, v160, v157
	v_fma_f32 v164, -v8, v161, v160
	v_fmac_f32_e32 v161, v164, v157
	v_fma_f32 v8, -v8, v161, v160
	v_div_fmas_f32 v8, v8, v157, v161
	v_div_fixup_f32 v4, v8, v4, 1.0
	v_div_scale_f32 v8, s[2:3], v3, v3, 1.0
	v_rcp_f32_e32 v157, v8
	s_nop 0
	v_fma_f32 v160, -v8, v157, 1.0
	v_fmac_f32_e32 v157, v160, v157
	v_div_scale_f32 v160, vcc, 1.0, v3, 1.0
	v_mul_f32_e32 v161, v160, v157
	v_fma_f32 v164, -v8, v161, v160
	v_fmac_f32_e32 v161, v164, v157
	v_fma_f32 v8, -v8, v161, v160
	v_div_fmas_f32 v8, v8, v157, v161
	v_div_fixup_f32 v3, v8, v3, 1.0
	v_div_scale_f32 v8, s[2:3], v2, v2, 1.0
	v_rcp_f32_e32 v157, v8
	s_nop 0
	v_fma_f32 v160, -v8, v157, 1.0
	v_fmac_f32_e32 v157, v160, v157
	v_div_scale_f32 v160, vcc, 1.0, v2, 1.0
	v_mul_f32_e32 v161, v160, v157
	v_fma_f32 v164, -v8, v161, v160
	v_fmac_f32_e32 v161, v164, v157
	v_fma_f32 v8, -v8, v161, v160
	v_div_fmas_f32 v8, v8, v157, v161
	v_div_fixup_f32 v2, v8, v2, 1.0
	v_div_scale_f32 v8, s[2:3], v1, v1, 1.0
	v_rcp_f32_e32 v157, v8
	s_nop 0
	v_fma_f32 v160, -v8, v157, 1.0
	v_fmac_f32_e32 v157, v160, v157
	v_div_scale_f32 v160, vcc, 1.0, v1, 1.0
	v_mul_f32_e32 v161, v160, v157
	v_fma_f32 v164, -v8, v161, v160
	v_fmac_f32_e32 v161, v164, v157
	v_fma_f32 v8, -v8, v161, v160
	v_div_fmas_f32 v8, v8, v157, v161
	v_div_fixup_f32 v1, v8, v1, 1.0
	v_div_scale_f32 v8, s[2:3], v0, v0, 1.0
	v_rcp_f32_e32 v157, v8
	s_mov_b64 s[2:3], 0
	v_fma_f32 v160, -v8, v157, 1.0
	v_fmac_f32_e32 v157, v160, v157
	v_div_scale_f32 v160, vcc, 1.0, v0, 1.0
	v_mul_f32_e32 v161, v160, v157
	v_fma_f32 v164, -v8, v161, v160
	v_fmac_f32_e32 v161, v164, v157
	v_fma_f32 v8, -v8, v161, v160
	v_div_fmas_f32 v8, v8, v157, v161
	v_div_fixup_f32 v0, v8, v0, 1.0
;     __device__ __forceinline__ void operator()(AccMut acc, const Unit& u, int wr, int wc, int, int) const {
;     ...
;                     if (u.seg < 2) {
;                         const v4u ga = *(const v4u*)(gp + u.seg * D), gb = *(const v4u*)(gp + (u.seg + 1) * D);
;                         const float la[8] = {bflo(ga.x), bfhi(ga.x), bflo(ga.y), bfhi(ga.y), bflo(ga.z), bfhi(ga.z), bflo(ga.w), bfhi(ga.w)};
;                         const float lb[8] = {bflo(gb.x), bfhi(gb.x), bflo(gb.y), bfhi(gb.y), bflo(gb.z), bfhi(gb.z), bflo(gb.w), bfhi(gb.w)};
; #pragma unroll
;                         for (int j = 0; j < 8; ++j) { const float ea = __expf(-fminf(fmaxf(la[j], -30.f), 30.f)), eb = __expf(-fminf(fmaxf(lb[j], -30.f), 30.f)); sc[j] = (1.0f + eb) * __builtin_amdgcn_rcpf(1.0f + ea); }
.LBB0_1008:
	s_andn2_b64 vcc, exec, s[2:3]
	s_cbranch_vccnz .LBB0_1010
	s_lshl_b32 s96, s50, 12
	v_lshl_add_u64 v[4:5], v[158:159], 0, s[96:97]
	global_load_dwordx4 v[0:3], v[4:5], off nt
	v_add_co_u32_e32 v4, vcc, 0x1000, v4
	s_nop 1
	v_addc_co_u32_e32 v5, vcc, 0, v5, vcc
	global_load_dwordx4 v[4:7], v[4:5], off nt
	s_waitcnt vmcnt(1)
	v_lshlrev_b32_e32 v8, 16, v0
	v_lshlrev_b32_e32 v157, 16, v1
	v_and_b32_e32 v0, 0xffff0000, v0
	v_and_b32_e32 v1, 0xffff0000, v1
	v_lshlrev_b32_e32 v158, 16, v2
	v_lshlrev_b32_e32 v159, 16, v3
	v_and_b32_e32 v167, 0xffff0000, v3
	v_max_f32_e32 v3, v8, v8
	v_max_f32_e32 v8, v157, v157
	v_max_f32_e32 v0, v0, v0
	v_max_f32_e32 v1, v1, v1
	v_max_f32_e32 v157, v158, v158
	v_max_f32_e32 v158, v159, v159
	v_med3_f32 v8, v8, s54, v223
	v_med3_f32 v3, v3, s54, v223
	v_med3_f32 v0, v0, s54, v223
	v_med3_f32 v1, v1, s54, v223
	v_med3_f32 v158, v158, s54, v223
	v_mul_f32_e32 v8, 0xbfb8aa3b, v8
	v_and_b32_e32 v2, 0xffff0000, v2
	v_mul_f32_e32 v3, 0xbfb8aa3b, v3
	v_mul_f32_e32 v0, 0xbfb8aa3b, v0
	v_mul_f32_e32 v1, 0xbfb8aa3b, v1
	v_mul_f32_e32 v158, 0xbfb8aa3b, v158
	v_exp_f32_e32 v8, v8
	v_max_f32_e32 v2, v2, v2
	v_exp_f32_e32 v165, v3
	v_exp_f32_e32 v166, v158
	v_med3_f32 v2, v2, s54, v223
	v_mul_f32_e32 v2, 0xbfb8aa3b, v2
	v_add_f32_e32 v8, 1.0, v8
	v_med3_f32 v157, v157, s54, v223
	v_mul_f32_e32 v157, 0xbfb8aa3b, v157
	v_exp_f32_e32 v157, v157
	s_waitcnt vmcnt(0)
	v_lshlrev_b32_e32 v159, 16, v4
	v_and_b32_e32 v4, 0xffff0000, v4
	v_lshlrev_b32_e32 v160, 16, v5
	v_max_f32_e32 v159, v159, v159
	v_max_f32_e32 v4, v4, v4
	v_max_f32_e32 v160, v160, v160
	v_and_b32_e32 v5, 0xffff0000, v5
	v_med3_f32 v3, v159, s54, v223
	v_exp_f32_e32 v159, v0
	v_med3_f32 v0, v4, s54, v223
	v_med3_f32 v4, v160, s54, v223
	v_exp_f32_e32 v160, v1
	v_lshlrev_b32_e32 v161, 16, v6
	v_and_b32_e32 v6, 0xffff0000, v6
	v_lshlrev_b32_e32 v164, 16, v7
	v_max_f32_e32 v5, v5, v5
	v_max_f32_e32 v161, v161, v161
	v_max_f32_e32 v6, v6, v6
	v_max_f32_e32 v164, v164, v164
	v_med3_f32 v1, v5, s54, v223
	v_med3_f32 v5, v161, s54, v223
	v_exp_f32_e32 v161, v2
	v_med3_f32 v2, v6, s54, v223
	v_med3_f32 v6, v164, s54, v223
	v_mul_f32_e32 v3, 0xbfb8aa3b, v3
	v_mul_f32_e32 v164, 0xbfb8aa3b, v1
	v_mul_f32_e32 v158, 0xbfb8aa3b, v0
	v_exp_f32_e32 v0, v3
	v_exp_f32_e32 v3, v164
	v_add_f32_e32 v164, 1.0, v160
	v_rcp_f32_e32 v160, v8
	v_add_f32_e32 v8, 1.0, v166
	v_rcp_f32_e32 v166, v8
	v_max_f32_e32 v8, v167, v167
	v_med3_f32 v8, v8, s54, v223
	v_mul_f32_e32 v8, 0xbfb8aa3b, v8
	v_and_b32_e32 v7, 0xffff0000, v7
	v_exp_f32_e32 v8, v8
	v_max_f32_e32 v7, v7, v7
	v_med3_f32 v7, v7, s54, v223
	v_mul_f32_e32 v4, 0xbfb8aa3b, v4
	v_mul_f32_e32 v5, 0xbfb8aa3b, v5
	v_mul_f32_e32 v168, 0xbfb8aa3b, v2
	v_mul_f32_e32 v6, 0xbfb8aa3b, v6
	v_mul_f32_e32 v7, 0xbfb8aa3b, v7
	v_exp_f32_e32 v1, v158
	v_exp_f32_e32 v2, v4
	v_exp_f32_e32 v4, v5
	v_exp_f32_e32 v5, v168
	v_add_f32_e32 v158, 1.0, v165
	v_add_f32_e32 v159, 1.0, v159
	v_add_f32_e32 v157, 1.0, v157
	v_add_f32_e32 v165, 1.0, v161
	v_exp_f32_e32 v6, v6
	v_exp_f32_e32 v7, v7
	v_add_f32_e32 v8, 1.0, v8
	v_rcp_f32_e32 v158, v158
	v_rcp_f32_e32 v159, v159
	v_rcp_f32_e32 v161, v164
	v_rcp_f32_e32 v164, v157
	v_rcp_f32_e32 v165, v165
	v_rcp_f32_e32 v167, v8
	v_pk_add_f32 v[0:1], v[0:1], 1.0 op_sel_hi:[1,0]
	v_pk_add_f32 v[2:3], v[2:3], 1.0 op_sel_hi:[1,0]
	v_pk_add_f32 v[4:5], v[4:5], 1.0 op_sel_hi:[1,0]
	v_pk_add_f32 v[6:7], v[6:7], 1.0 op_sel_hi:[1,0]
	v_pk_mul_f32 v[4:5], v[4:5], v[164:165]
	v_pk_mul_f32 v[6:7], v[6:7], v[166:167]
	v_pk_mul_f32 v[2:3], v[2:3], v[160:161]
	v_pk_mul_f32 v[0:1], v[0:1], v[158:159]

; __device__ __forceinline__ float sigmoidf_(float x) { return 1.0f / (1.0f + __expf(-x)); }
;     __device__ __forceinline__ void operator()(AccMut acc, const Unit& u, int wr, int wc, int, int) const {
;     ...
;                     const int row = row0 + ai * 128 + m * 16, col = col0 + bj * 128;
;                     const bf16* gp = PROJ + (size_t)row * DINP + GATE_OFF + col;
;                     float sc[8];
;                     if (u.seg < 2) {
;                         const v4u ga = *(const v4u*)(gp + u.seg * D), gb = *(const v4u*)(gp + (u.seg + 1) * D);
;                         const float la[8] = {bflo(ga.x), bfhi(ga.x), bflo(ga.y), bfhi(ga.y), bflo(ga.z), bfhi(ga.z), bflo(ga.w), bfhi(ga.w)};
;                         const float lb[8] = {bflo(gb.x), bfhi(gb.x), bflo(gb.y), bfhi(gb.y), bflo(gb.z), bfhi(gb.z), bflo(gb.w), bfhi(gb.w)};
; #pragma unroll
;                         for (int j = 0; j < 8; ++j) { const float ea = __expf(-fminf(fmaxf(la[j], -30.f), 30.f)), eb = __expf(-fminf(fmaxf(lb[j], -30.f), 30.f)); sc[j] = (1.0f + eb) * __builtin_amdgcn_rcpf(1.0f + ea); }
;                     } else {
;                         const v4u ga = *(const v4u*)(gp + 2 * D);
;                         const float la[8] = {bflo(ga.x), bfhi(ga.x), bflo(ga.y), bfhi(ga.y), bflo(ga.z), bfhi(ga.z), bflo(ga.w), bfhi(ga.w)};
; #pragma unroll
;                         for (int j = 0; j < 8; ++j) sc[j] = sigmoidf_(la[j]);
.LBB0_1013:
	v_lshl_add_u64 v[0:1], v[152:153], 1, v[154:155]
	v_add_co_u32_e32 v0, vcc, 0x2000, v0
	s_nop 1
	v_addc_co_u32_e32 v1, vcc, 0, v1, vcc
	global_load_dwordx4 v[0:3], v[0:1], off nt
	s_waitcnt vmcnt(0)
	v_lshlrev_b32_e32 v6, 16, v1
	v_and_b32_e32 v7, 0xffff0000, v1
	v_lshlrev_b32_e32 v157, 16, v3
	v_and_b32_e32 v158, 0xffff0000, v3
	v_lshlrev_b32_e32 v8, 16, v2
	v_and_b32_e32 v156, 0xffff0000, v2
	v_mul_f32_e32 v2, 0xbfb8aa3b, v6
	v_mul_f32_e32 v3, 0xbfb8aa3b, v7
	v_mul_f32_e32 v6, 0xbfb8aa3b, v157
	v_mul_f32_e32 v7, 0xbfb8aa3b, v158
	v_exp_f32_e32 v6, v6
	v_exp_f32_e32 v7, v7
	v_lshlrev_b32_e32 v4, 16, v0
	v_and_b32_e32 v5, 0xffff0000, v0
	v_mul_f32_e32 v0, 0xbfb8aa3b, v4
	v_pk_add_f32 v[6:7], v[6:7], 1.0 op_sel_hi:[1,0]
	v_mul_f32_e32 v4, 0xbfb8aa3b, v8
	v_div_scale_f32 v8, s[2:3], v7, v7, 1.0
	v_mul_f32_e32 v1, 0xbfb8aa3b, v5
	v_mul_f32_e32 v5, 0xbfb8aa3b, v156
	v_rcp_f32_e32 v156, v8
	v_exp_f32_e32 v4, v4
	v_exp_f32_e32 v5, v5
	v_exp_f32_e32 v2, v2
	v_fma_f32 v157, -v8, v156, 1.0
	v_fmac_f32_e32 v156, v157, v156
	v_div_scale_f32 v157, vcc, 1.0, v7, 1.0
	v_mul_f32_e32 v158, v157, v156
	v_fma_f32 v159, -v8, v158, v157
	v_fmac_f32_e32 v158, v159, v156
	v_fma_f32 v8, -v8, v158, v157
	v_div_fmas_f32 v8, v8, v156, v158
	v_div_fixup_f32 v7, v8, v7, 1.0
	v_div_scale_f32 v8, s[2:3], v6, v6, 1.0
	v_rcp_f32_e32 v156, v8
	v_pk_add_f32 v[4:5], v[4:5], 1.0 op_sel_hi:[1,0]
	v_exp_f32_e32 v3, v3
	v_exp_f32_e32 v0, v0
	v_fma_f32 v157, -v8, v156, 1.0
	v_fmac_f32_e32 v156, v157, v156
	v_div_scale_f32 v157, vcc, 1.0, v6, 1.0
	v_mul_f32_e32 v158, v157, v156
	v_fma_f32 v159, -v8, v158, v157
	v_fmac_f32_e32 v158, v159, v156
	v_fma_f32 v8, -v8, v158, v157
	v_div_fmas_f32 v8, v8, v156, v158
	v_div_fixup_f32 v6, v8, v6, 1.0
	v_div_scale_f32 v8, s[2:3], v5, v5, 1.0
	v_rcp_f32_e32 v156, v8
	v_pk_add_f32 v[2:3], v[2:3], 1.0 op_sel_hi:[1,0]
	v_exp_f32_e32 v1, v1
	v_fma_f32 v157, -v8, v156, 1.0
	v_fmac_f32_e32 v156, v157, v156
	v_div_scale_f32 v157, vcc, 1.0, v5, 1.0
	v_mul_f32_e32 v158, v157, v156
	v_fma_f32 v159, -v8, v158, v157
	v_fmac_f32_e32 v158, v159, v156
	v_fma_f32 v8, -v8, v158, v157
	v_div_fmas_f32 v8, v8, v156, v158
	v_div_fixup_f32 v5, v8, v5, 1.0
	v_div_scale_f32 v8, s[2:3], v4, v4, 1.0
	v_rcp_f32_e32 v156, v8
	v_pk_add_f32 v[0:1], v[0:1], 1.0 op_sel_hi:[1,0]
	v_fma_f32 v157, -v8, v156, 1.0
	v_fmac_f32_e32 v156, v157, v156
	v_div_scale_f32 v157, vcc, 1.0, v4, 1.0
	v_mul_f32_e32 v158, v157, v156
	v_fma_f32 v159, -v8, v158, v157
	v_fmac_f32_e32 v158, v159, v156
	v_fma_f32 v8, -v8, v158, v157
	v_div_fmas_f32 v8, v8, v156, v158
	v_div_fixup_f32 v4, v8, v4, 1.0
	v_div_scale_f32 v8, s[2:3], v3, v3, 1.0
	v_rcp_f32_e32 v156, v8
	s_nop 0
	v_fma_f32 v157, -v8, v156, 1.0
	v_fmac_f32_e32 v156, v157, v156
	v_div_scale_f32 v157, vcc, 1.0, v3, 1.0
	v_mul_f32_e32 v158, v157, v156
	v_fma_f32 v159, -v8, v158, v157
	v_fmac_f32_e32 v158, v159, v156
	v_fma_f32 v8, -v8, v158, v157
	v_div_fmas_f32 v8, v8, v156, v158
	v_div_fixup_f32 v3, v8, v3, 1.0
	v_div_scale_f32 v8, s[2:3], v2, v2, 1.0
	v_rcp_f32_e32 v156, v8
	s_nop 0
	v_fma_f32 v157, -v8, v156, 1.0
	v_fmac_f32_e32 v156, v157, v156
	v_div_scale_f32 v157, vcc, 1.0, v2, 1.0
	v_mul_f32_e32 v158, v157, v156
	v_fma_f32 v159, -v8, v158, v157
	v_fmac_f32_e32 v158, v159, v156
	v_fma_f32 v8, -v8, v158, v157
	v_div_fmas_f32 v8, v8, v156, v158
	v_div_fixup_f32 v2, v8, v2, 1.0
	v_div_scale_f32 v8, s[2:3], v1, v1, 1.0
	v_rcp_f32_e32 v156, v8
	s_nop 0
	v_fma_f32 v157, -v8, v156, 1.0
	v_fmac_f32_e32 v156, v157, v156
	v_div_scale_f32 v157, vcc, 1.0, v1, 1.0
	v_mul_f32_e32 v158, v157, v156
	v_fma_f32 v159, -v8, v158, v157
	v_fmac_f32_e32 v158, v159, v156
	v_fma_f32 v8, -v8, v158, v157
	v_div_fmas_f32 v8, v8, v156, v158
	v_div_fixup_f32 v1, v8, v1, 1.0
	v_div_scale_f32 v8, s[2:3], v0, v0, 1.0
	v_rcp_f32_e32 v156, v8
	s_mov_b64 s[2:3], 0
	v_fma_f32 v157, -v8, v156, 1.0
	v_fmac_f32_e32 v156, v157, v156
	v_div_scale_f32 v157, vcc, 1.0, v0, 1.0
	v_mul_f32_e32 v158, v157, v156
	v_fma_f32 v159, -v8, v158, v157
	v_fmac_f32_e32 v158, v159, v156
	v_fma_f32 v8, -v8, v158, v157
	v_div_fmas_f32 v8, v8, v156, v158
	v_div_fixup_f32 v0, v8, v0, 1.0
;     __device__ __forceinline__ void operator()(AccMut acc, const Unit& u, int wr, int wc, int, int) const {
;     ...
;                     if (u.seg < 2) {
;                         const v4u ga = *(const v4u*)(gp + u.seg * D), gb = *(const v4u*)(gp + (u.seg + 1) * D);
;                         const float la[8] = {bflo(ga.x), bfhi(ga.x), bflo(ga.y), bfhi(ga.y), bflo(ga.z), bfhi(ga.z), bflo(ga.w), bfhi(ga.w)};
;                         const float lb[8] = {bflo(gb.x), bfhi(gb.x), bflo(gb.y), bfhi(gb.y), bflo(gb.z), bfhi(gb.z), bflo(gb.w), bfhi(gb.w)};
; #pragma unroll
;                         for (int j = 0; j < 8; ++j) { const float ea = __expf(-fminf(fmaxf(la[j], -30.f), 30.f)), eb = __expf(-fminf(fmaxf(lb[j], -30.f), 30.f)); sc[j] = (1.0f + eb) * __builtin_amdgcn_rcpf(1.0f + ea); }
.LBB0_1014:
	s_andn2_b64 vcc, exec, s[2:3]
	s_cbranch_vccnz .LBB0_1016
	s_lshl_b32 s96, s50, 12
	v_lshl_add_u64 v[0:1], v[154:155], 0, s[96:97]
	v_lshl_add_u64 v[4:5], v[152:153], 1, v[0:1]
	global_load_dwordx4 v[0:3], v[4:5], off nt
	v_add_co_u32_e32 v4, vcc, 0x1000, v4
	s_nop 1
	v_addc_co_u32_e32 v5, vcc, 0, v5, vcc
	global_load_dwordx4 v[4:7], v[4:5], off nt
	s_waitcnt vmcnt(1)
	v_lshlrev_b32_e32 v8, 16, v0
	v_and_b32_e32 v0, 0xffff0000, v0
	v_lshlrev_b32_e32 v152, 16, v1
	v_and_b32_e32 v1, 0xffff0000, v1
	v_lshlrev_b32_e32 v153, 16, v2
	v_and_b32_e32 v2, 0xffff0000, v2
	v_lshlrev_b32_e32 v154, 16, v3
	v_and_b32_e32 v159, 0xffff0000, v3
	v_max_f32_e32 v3, v8, v8
	v_max_f32_e32 v0, v0, v0
	v_max_f32_e32 v8, v152, v152
	v_max_f32_e32 v1, v1, v1
	v_max_f32_e32 v152, v153, v153
	v_max_f32_e32 v2, v2, v2
	v_max_f32_e32 v153, v154, v154
	v_med3_f32 v3, v3, s54, v223
	v_med3_f32 v0, v0, s54, v223
	v_med3_f32 v8, v8, s54, v223
	v_med3_f32 v1, v1, s54, v223
	v_med3_f32 v152, v152, s54, v223
	v_med3_f32 v2, v2, s54, v223
	v_med3_f32 v153, v153, s54, v223
	v_mul_f32_e32 v3, 0xbfb8aa3b, v3
	v_mul_f32_e32 v0, 0xbfb8aa3b, v0
	v_mul_f32_e32 v8, 0xbfb8aa3b, v8
	v_mul_f32_e32 v1, 0xbfb8aa3b, v1
	v_mul_f32_e32 v152, 0xbfb8aa3b, v152
	v_mul_f32_e32 v2, 0xbfb8aa3b, v2
	v_mul_f32_e32 v153, 0xbfb8aa3b, v153
	v_exp_f32_e32 v158, v3
	v_exp_f32_e32 v8, v8
	v_exp_f32_e32 v152, v152
	v_exp_f32_e32 v160, v153
	v_add_f32_e32 v8, 1.0, v8
	s_waitcnt vmcnt(0)
	v_lshlrev_b32_e32 v154, 16, v4
	v_and_b32_e32 v4, 0xffff0000, v4
	v_lshlrev_b32_e32 v155, 16, v5
	v_and_b32_e32 v5, 0xffff0000, v5
	v_lshlrev_b32_e32 v156, 16, v6
	v_max_f32_e32 v154, v154, v154
	v_max_f32_e32 v4, v4, v4
	v_max_f32_e32 v155, v155, v155
	v_max_f32_e32 v5, v5, v5
	v_max_f32_e32 v156, v156, v156
	v_med3_f32 v3, v154, s54, v223
	v_exp_f32_e32 v154, v0
	v_med3_f32 v0, v4, s54, v223
	v_med3_f32 v4, v155, s54, v223
	v_exp_f32_e32 v155, v1
	v_med3_f32 v1, v5, s54, v223
	v_med3_f32 v5, v156, s54, v223
	v_exp_f32_e32 v156, v2
	v_and_b32_e32 v6, 0xffff0000, v6
	v_lshlrev_b32_e32 v157, 16, v7
	v_max_f32_e32 v6, v6, v6
	v_max_f32_e32 v157, v157, v157
	v_mul_f32_e32 v153, 0xbfb8aa3b, v0
	v_med3_f32 v2, v6, s54, v223
	v_med3_f32 v6, v157, s54, v223
	v_mul_f32_e32 v3, 0xbfb8aa3b, v3
	v_mul_f32_e32 v157, 0xbfb8aa3b, v1
	v_exp_f32_e32 v1, v153
	v_add_f32_e32 v153, 1.0, v158
	v_add_f32_e32 v154, 1.0, v154
	v_exp_f32_e32 v0, v3
	v_exp_f32_e32 v3, v157
	v_add_f32_e32 v157, 1.0, v152
	v_add_f32_e32 v158, 1.0, v156
	v_rcp_f32_e32 v152, v153
	v_rcp_f32_e32 v153, v154
	v_rcp_f32_e32 v154, v8
	v_add_f32_e32 v8, 1.0, v160
	v_rcp_f32_e32 v156, v157
	v_rcp_f32_e32 v157, v158
	v_rcp_f32_e32 v158, v8
	v_max_f32_e32 v8, v159, v159
	v_med3_f32 v8, v8, s54, v223
	v_mul_f32_e32 v8, 0xbfb8aa3b, v8
	v_and_b32_e32 v7, 0xffff0000, v7
	v_exp_f32_e32 v8, v8
	v_max_f32_e32 v7, v7, v7
	v_med3_f32 v7, v7, s54, v223
	v_mul_f32_e32 v4, 0xbfb8aa3b, v4
	v_mul_f32_e32 v5, 0xbfb8aa3b, v5
	v_mul_f32_e32 v161, 0xbfb8aa3b, v2
	v_mul_f32_e32 v6, 0xbfb8aa3b, v6
	v_mul_f32_e32 v7, 0xbfb8aa3b, v7
	v_exp_f32_e32 v2, v4
	v_exp_f32_e32 v4, v5
	v_exp_f32_e32 v5, v161
	v_add_f32_e32 v155, 1.0, v155
	v_exp_f32_e32 v6, v6
	v_exp_f32_e32 v7, v7
	v_add_f32_e32 v8, 1.0, v8
	v_rcp_f32_e32 v155, v155
	v_rcp_f32_e32 v159, v8
	v_pk_add_f32 v[0:1], v[0:1], 1.0 op_sel_hi:[1,0]
	v_pk_add_f32 v[2:3], v[2:3], 1.0 op_sel_hi:[1,0]
	v_pk_add_f32 v[4:5], v[4:5], 1.0 op_sel_hi:[1,0]
	v_pk_add_f32 v[6:7], v[6:7], 1.0 op_sel_hi:[1,0]
	v_pk_mul_f32 v[4:5], v[4:5], v[156:157]
	v_pk_mul_f32 v[6:7], v[6:7], v[158:159]
	v_pk_mul_f32 v[2:3], v[2:3], v[154:155]
	v_pk_mul_f32 v[0:1], v[0:1], v[152:153]
